# best + loader segments of all five K-loops at s_setprio 2 until their vmcnt wait
# baseline (speedup 1.0000x reference)
; #define PG8_STAGE(bufoff, gbase, voff) do { _Pragma("unroll") for (int _i = 0; _i < 2; ++_i) \
;         __builtin_amdgcn_global_load_lds((const unsigned*)((const char*)(gbase) + (voff)[_i]), (PG8_LAS unsigned*)(lds + (bufoff) + ldsw + _i * 8192), 16, 0, 0); } while (0)
; #define PG8_LDA(dst, b, h) do { _Pragma("unroll") for (int m = 0; m < 4; ++m) _Pragma("unroll") for (int k = 0; k < 2; ++k) dst[m][k] = *(const PG8_LAS bf16x8*)(lds + PG8_SA(b, h) + aoff + m * 2048 + k * 1024); } while (0)
; #define PG8_LDB(dst, b, h) do { _Pragma("unroll") for (int n = 0; n < 2; ++n) _Pragma("unroll") for (int k = 0; k < 2; ++k) dst[n][k] = *(const PG8_LAS bf16x8*)(lds + PG8_SB(b, h) + boff + n * 2048 + k * 1024); } while (0)
; #define PG8_MMA(ai, bj, At, Bt) do { __builtin_amdgcn_s_setprio(1); _Pragma("unroll") for (int m = 0; m < 4; ++m) _Pragma("unroll") for (int n = 0; n < 2; ++n) _Pragma("unroll") for (int k = 0; k < 2; ++k) \
;         acc[ai][bj][m][n] = __builtin_amdgcn_mfma_f32_16x16x32_bf16(Bt[n][k], At[m][k], acc[ai][bj][m][n], 0, 0, 0); __builtin_amdgcn_s_setprio(0); } while (0)
; #define PG8_WAIT_V(n) asm volatile("s_waitcnt vmcnt(" #n ")" ::: "memory")
; #define PG8_WAIT_L(n) asm volatile("s_waitcnt lgkmcnt(" #n ")" ::: "memory")
; #define PG8_BAR __builtin_amdgcn_s_barrier()
; template <class Epi, class Sched, bool ALIGN_EPI = false, bool SP2 = false>
; __device__ __forceinline__ void gemm_phase(PG8_LAS unsigned char* lds, const Gemm g, const Sched& S, const Epi& E) {
;     ...
;             const char* a1 = cA + (size_t)(t + 1) * kstep;
;             const char* a2 = last ? nA : cA + (size_t)(t + 2) * kstep; const char* b2 = last ? nB : cB + (size_t)(t + 2) * kstep;
;             const char* a3 = a2 + kstep; const char* b3 = b2 + kstep;
;             if (last && has_next) S.a_ready(nxt);
;             if constexpr (SP2) {
;             PG8_LDB(B0, 0, 0); PG8_LDB(B1, 0, 1); PG8_SCHED; PG8_LDA(At, 0, 0); PG8_STAGE(PG8_SA(1, 1), a1 + hstep, voffA);
;             PG8_WAIT_V(8); PG8_WAIT_L(0); PG8_BAR; PG8_MMA(0, 0, At, B0); PG8_MMA(0, 1, At, B1); PG8_BAR; PG8_SCHED;
;             PG8_LDA(At, 0, 1); PG8_STAGE(PG8_SB(0, 0), b2, voffB); PG8_STAGE(PG8_SB(0, 1), b2 + hstep, voffB); PG8_STAGE(PG8_SA(0, 0), a2, voffA);
;             PG8_WAIT_V(8); PG8_WAIT_L(0); PG8_BAR; PG8_MMA(1, 0, At, B0); PG8_MMA(1, 1, At, B1); PG8_BAR; PG8_SCHED;
.LBB0_332:
	s_setprio 2
	ds_read_b128 v[132:135], v213
	ds_read_b128 v[136:139], v213 offset:1024
	ds_read_b128 v[140:143], v213 offset:2048
	ds_read_b128 v[144:147], v213 offset:3072
	ds_read_b128 v[148:151], v214
	ds_read_b128 v[152:155], v214 offset:1024
	ds_read_b128 v[156:159], v214 offset:2048
	ds_read_b128 v[178:181], v214 offset:3072
	s_add_u32 s2, s0, 0xfff80080
	s_addc_u32 s3, s1, -1
	s_cmp_eq_u32 s95, 28
	s_cselect_b32 s5, s7, s3
	s_cselect_b32 s4, s33, s2
	s_cselect_b32 s3, s53, s85
	s_cselect_b32 s2, s55, s84
	v_lshl_add_u64 v[160:161], s[0:1], 0, v[172:173]
	s_add_i32 m0, s63, 0xc000
	ds_read_b128 v[182:185], v215
	ds_read_b128 v[188:191], v215 offset:1024
	ds_read_b128 v[192:195], v215 offset:2048
	ds_read_b128 v[196:199], v215 offset:3072
	ds_read_b128 v[200:203], v215 offset:4096
	ds_read_b128 v[204:207], v215 offset:5120
	ds_read_b128 v[218:221], v215 offset:6144
	ds_read_b128 v[222:225], v215 offset:7168
	global_load_lds_dwordx4 v[160:161], off
	v_lshl_add_u64 v[160:161], s[0:1], 0, v[174:175]
	s_add_i32 m0, s63, 0xe000
	s_nop 0
	global_load_lds_dwordx4 v[160:161], off
	s_setprio 0
	s_waitcnt vmcnt(8)
	s_waitcnt lgkmcnt(0)
	s_barrier
	s_setprio 1
	s_waitcnt lgkmcnt(0)
	v_mfma_f32_16x16x32_bf16 v[126:129], v[132:135], v[182:185], v[126:129]
	v_mfma_f32_16x16x32_bf16 v[122:125], v[140:143], v[182:185], v[122:125]
	v_mfma_f32_16x16x32_bf16 v[118:121], v[132:135], v[192:195], v[118:121]
	v_mfma_f32_16x16x32_bf16 v[110:113], v[140:143], v[192:195], v[110:113]
	v_mfma_f32_16x16x32_bf16 v[102:105], v[132:135], v[200:203], v[102:105]
	v_mfma_f32_16x16x32_bf16 v[94:97], v[140:143], v[200:203], v[94:97]
	v_mfma_f32_16x16x32_bf16 v[86:89], v[132:135], v[218:221], v[86:89]
	v_mfma_f32_16x16x32_bf16 v[78:81], v[140:143], v[218:221], v[78:81]
	v_mfma_f32_16x16x32_bf16 v[126:129], v[136:139], v[188:191], v[126:129]
	v_mfma_f32_16x16x32_bf16 v[122:125], v[144:147], v[188:191], v[122:125]
	v_mfma_f32_16x16x32_bf16 v[118:121], v[136:139], v[196:199], v[118:121]
	v_mfma_f32_16x16x32_bf16 v[110:113], v[144:147], v[196:199], v[110:113]
	v_mfma_f32_16x16x32_bf16 v[102:105], v[136:139], v[204:207], v[102:105]
	v_mfma_f32_16x16x32_bf16 v[94:97], v[144:147], v[204:207], v[94:97]
	v_mfma_f32_16x16x32_bf16 v[86:89], v[136:139], v[222:225], v[86:89]
	v_mfma_f32_16x16x32_bf16 v[78:81], v[144:147], v[222:225], v[78:81]
	s_setprio 0
	s_setprio 1
	v_mfma_f32_16x16x32_bf16 v[114:117], v[148:151], v[182:185], v[114:117]
	v_mfma_f32_16x16x32_bf16 v[106:109], v[156:159], v[182:185], v[106:109]
	v_mfma_f32_16x16x32_bf16 v[98:101], v[148:151], v[192:195], v[98:101]
	v_mfma_f32_16x16x32_bf16 v[90:93], v[156:159], v[192:195], v[90:93]
	v_mfma_f32_16x16x32_bf16 v[82:85], v[148:151], v[200:203], v[82:85]
	v_mfma_f32_16x16x32_bf16 v[74:77], v[156:159], v[200:203], v[74:77]
	v_mfma_f32_16x16x32_bf16 v[70:73], v[148:151], v[218:221], v[70:73]
	v_mfma_f32_16x16x32_bf16 v[66:69], v[156:159], v[218:221], v[66:69]
	v_mfma_f32_16x16x32_bf16 v[114:117], v[152:155], v[188:191], v[114:117]
	v_mfma_f32_16x16x32_bf16 v[106:109], v[178:181], v[188:191], v[106:109]
	v_mfma_f32_16x16x32_bf16 v[98:101], v[152:155], v[196:199], v[98:101]
	v_mfma_f32_16x16x32_bf16 v[90:93], v[178:181], v[196:199], v[90:93]
	v_mfma_f32_16x16x32_bf16 v[82:85], v[152:155], v[204:207], v[82:85]
	v_mfma_f32_16x16x32_bf16 v[74:77], v[178:181], v[204:207], v[74:77]
	v_mfma_f32_16x16x32_bf16 v[70:73], v[152:155], v[222:225], v[70:73]
	v_mfma_f32_16x16x32_bf16 v[66:69], v[178:181], v[222:225], v[66:69]
	s_setprio 0
	s_barrier
	s_setprio 2
	s_add_i32 s96, s81, s66
	v_lshl_add_u64 v[160:161], s[2:3], 0, v[164:165]
	s_mov_b32 m0, s96
	ds_read_b128 v[182:185], v215 offset:16384
	ds_read_b128 v[188:191], v215 offset:17408
	ds_read_b128 v[192:195], v215 offset:18432
	ds_read_b128 v[196:199], v215 offset:19456
	ds_read_b128 v[200:203], v215 offset:20480
	ds_read_b128 v[204:207], v215 offset:21504
	ds_read_b128 v[218:221], v215 offset:22528
	ds_read_b128 v[222:225], v215 offset:23552
	global_load_lds_dwordx4 v[160:161], off
	s_add_i32 m0, s96, 0x2000
	s_add_u32 s96, s2, 0x80000
	v_lshl_add_u64 v[208:209], s[2:3], 0, v[168:169]
	s_addc_u32 s97, s3, 0
	s_add_i32 vcc_lo, s82, s66
	global_load_lds_dwordx4 v[208:209], off
	v_lshl_add_u64 v[226:227], s[96:97], 0, v[164:165]
	s_mov_b32 m0, vcc_lo
	v_lshl_add_u64 v[228:229], s[4:5], 0, v[166:167]
	global_load_lds_dwordx4 v[226:227], off
	v_lshl_add_u64 v[226:227], s[96:97], 0, v[168:169]
	s_add_i32 m0, vcc_lo, 0x2000
	s_nop 0
	global_load_lds_dwordx4 v[226:227], off
	v_lshl_add_u64 v[226:227], s[4:5], 0, v[162:163]
	s_mov_b32 m0, s63
	s_nop 0
	global_load_lds_dwordx4 v[226:227], off
	s_mov_b32 m0, s65
	s_nop 0
	global_load_lds_dwordx4 v[228:229], off
	s_setprio 0
	s_waitcnt vmcnt(8)
	s_waitcnt lgkmcnt(0)
	s_barrier
; #define PG8_STAGE(bufoff, gbase, voff) do { _Pragma("unroll") for (int _i = 0; _i < 2; ++_i) \
;         __builtin_amdgcn_global_load_lds((const unsigned*)((const char*)(gbase) + (voff)[_i]), (PG8_LAS unsigned*)(lds + (bufoff) + ldsw + _i * 8192), 16, 0, 0); } while (0)
; #define PG8_LDA(dst, b, h) do { _Pragma("unroll") for (int m = 0; m < 4; ++m) _Pragma("unroll") for (int k = 0; k < 2; ++k) dst[m][k] = *(const PG8_LAS bf16x8*)(lds + PG8_SA(b, h) + aoff + m * 2048 + k * 1024); } while (0)
; #define PG8_LDB(dst, b, h) do { _Pragma("unroll") for (int n = 0; n < 2; ++n) _Pragma("unroll") for (int k = 0; k < 2; ++k) dst[n][k] = *(const PG8_LAS bf16x8*)(lds + PG8_SB(b, h) + boff + n * 2048 + k * 1024); } while (0)
; #define PG8_MMA(ai, bj, At, Bt) do { __builtin_amdgcn_s_setprio(1); _Pragma("unroll") for (int m = 0; m < 4; ++m) _Pragma("unroll") for (int n = 0; n < 2; ++n) _Pragma("unroll") for (int k = 0; k < 2; ++k) \
;         acc[ai][bj][m][n] = __builtin_amdgcn_mfma_f32_16x16x32_bf16(Bt[n][k], At[m][k], acc[ai][bj][m][n], 0, 0, 0); __builtin_amdgcn_s_setprio(0); } while (0)
; #define PG8_WAIT_V(n) asm volatile("s_waitcnt vmcnt(" #n ")" ::: "memory")
; #define PG8_WAIT_L(n) asm volatile("s_waitcnt lgkmcnt(" #n ")" ::: "memory")
; #define PG8_BAR __builtin_amdgcn_s_barrier()
; #define PG8_SCHED __builtin_amdgcn_sched_barrier(0)
; #define PG8_STAGE(bufoff, gbase, voff) do { _Pragma("unroll") for (int _i = 0; _i < 2; ++_i) \
;         __builtin_amdgcn_global_load_lds((const unsigned*)((const char*)(gbase) + (voff)[_i]), (PG8_LAS unsigned*)(lds + (bufoff) + ldsw + _i * 8192), 16, 0, 0); } while (0)
; #define PG8_WAIT_V(n) asm volatile("s_waitcnt vmcnt(" #n ")" ::: "memory")
; #define PG8_WAIT_L(n) asm volatile("s_waitcnt lgkmcnt(" #n ")" ::: "memory")
; #define PG8_BAR __builtin_amdgcn_s_barrier()
; template <class Epi, class Sched, bool ALIGN_EPI = false, bool SP2 = false>
; __device__ __forceinline__ void gemm_phase(PG8_LAS unsigned char* lds, const Gemm g, const Sched& S, const Epi& E) {
;     ...
;             PG8_WAIT_V(8); PG8_WAIT_L(0); PG8_BAR; PG8_MMA(1, 0, At, B0); PG8_MMA(1, 1, At, B1); PG8_BAR; PG8_SCHED;
;             PG8_LDB(B0, 1, 0); PG8_LDB(B1, 1, 1); PG8_SCHED; PG8_LDA(At, 1, 0); PG8_STAGE(PG8_SA(0, 1), a2 + hstep, voffA);
;             PG8_WAIT_V(8); PG8_WAIT_L(0); PG8_BAR; PG8_MMA(0, 0, At, B0); PG8_MMA(0, 1, At, B1); PG8_BAR; PG8_SCHED;
	s_setprio 1
	s_waitcnt lgkmcnt(0)
	v_mfma_f32_16x16x32_bf16 v[62:65], v[132:135], v[182:185], v[62:65]
	v_mfma_f32_16x16x32_bf16 v[58:61], v[140:143], v[182:185], v[58:61]
	v_mfma_f32_16x16x32_bf16 v[54:57], v[132:135], v[192:195], v[54:57]
	v_mfma_f32_16x16x32_bf16 v[46:49], v[140:143], v[192:195], v[46:49]
	v_mfma_f32_16x16x32_bf16 v[38:41], v[132:135], v[200:203], v[38:41]
	v_mfma_f32_16x16x32_bf16 v[30:33], v[140:143], v[200:203], v[30:33]
	v_mfma_f32_16x16x32_bf16 v[22:25], v[132:135], v[218:221], v[22:25]
	v_mfma_f32_16x16x32_bf16 v[14:17], v[140:143], v[218:221], v[14:17]
	v_mfma_f32_16x16x32_bf16 v[62:65], v[136:139], v[188:191], v[62:65]
	v_mfma_f32_16x16x32_bf16 v[58:61], v[144:147], v[188:191], v[58:61]
	v_mfma_f32_16x16x32_bf16 v[54:57], v[136:139], v[196:199], v[54:57]
	v_mfma_f32_16x16x32_bf16 v[46:49], v[144:147], v[196:199], v[46:49]
	v_mfma_f32_16x16x32_bf16 v[38:41], v[136:139], v[204:207], v[38:41]
	v_mfma_f32_16x16x32_bf16 v[30:33], v[144:147], v[204:207], v[30:33]
	v_mfma_f32_16x16x32_bf16 v[22:25], v[136:139], v[222:225], v[22:25]
	v_mfma_f32_16x16x32_bf16 v[14:17], v[144:147], v[222:225], v[14:17]
	s_setprio 0
	s_setprio 1
	v_mfma_f32_16x16x32_bf16 v[50:53], v[148:151], v[182:185], v[50:53]
	v_mfma_f32_16x16x32_bf16 v[42:45], v[156:159], v[182:185], v[42:45]
	v_mfma_f32_16x16x32_bf16 v[34:37], v[148:151], v[192:195], v[34:37]
	v_mfma_f32_16x16x32_bf16 v[26:29], v[156:159], v[192:195], v[26:29]
	v_mfma_f32_16x16x32_bf16 v[18:21], v[148:151], v[200:203], v[18:21]
	v_mfma_f32_16x16x32_bf16 v[10:13], v[156:159], v[200:203], v[10:13]
	v_mfma_f32_16x16x32_bf16 v[6:9], v[148:151], v[218:221], v[6:9]
	v_mfma_f32_16x16x32_bf16 v[2:5], v[156:159], v[218:221], v[2:5]
	v_mfma_f32_16x16x32_bf16 v[50:53], v[152:155], v[188:191], v[50:53]
	v_mfma_f32_16x16x32_bf16 v[42:45], v[178:181], v[188:191], v[42:45]
	v_mfma_f32_16x16x32_bf16 v[34:37], v[152:155], v[196:199], v[34:37]
	v_mfma_f32_16x16x32_bf16 v[26:29], v[178:181], v[196:199], v[26:29]
	v_mfma_f32_16x16x32_bf16 v[18:21], v[152:155], v[204:207], v[18:21]
	v_mfma_f32_16x16x32_bf16 v[10:13], v[178:181], v[204:207], v[10:13]
	v_mfma_f32_16x16x32_bf16 v[6:9], v[152:155], v[222:225], v[6:9]
	v_mfma_f32_16x16x32_bf16 v[2:5], v[178:181], v[222:225], v[2:5]
	s_setprio 0
	s_barrier
	s_setprio 2
	s_add_i32 s96, 0, 0x18000
	v_add_u32_e32 v131, s96, v211
	s_add_i32 s97, 0, 0x1c000
	ds_read_b128 v[132:135], v131
	ds_read_b128 v[136:139], v131 offset:1024
	ds_read_b128 v[140:143], v131 offset:2048
	ds_read_b128 v[144:147], v131 offset:3072
	v_add_u32_e32 v131, s97, v211
	ds_read_b128 v[148:151], v131
	ds_read_b128 v[152:155], v131 offset:1024
	ds_read_b128 v[156:159], v131 offset:2048
	ds_read_b128 v[178:181], v131 offset:3072
	s_add_u32 s4, s4, 0x80000
	s_addc_u32 s5, s5, 0
	s_mov_b32 m0, s71
	v_lshl_add_u64 v[230:231], s[4:5], 0, v[162:163]
	ds_read_b128 v[182:185], v215 offset:32768
	ds_read_b128 v[188:191], v215 offset:33792
	ds_read_b128 v[192:195], v215 offset:34816
	ds_read_b128 v[196:199], v215 offset:35840
	ds_read_b128 v[200:203], v215 offset:36864
	ds_read_b128 v[204:207], v215 offset:37888
	ds_read_b128 v[218:221], v215 offset:38912
	ds_read_b128 v[222:225], v215 offset:39936
	global_load_lds_dwordx4 v[230:231], off
	v_lshl_add_u64 v[230:231], s[4:5], 0, v[166:167]
	s_mov_b32 m0, s72
	s_nop 0
	global_load_lds_dwordx4 v[230:231], off
	s_setprio 0
	s_waitcnt vmcnt(8)
	s_waitcnt lgkmcnt(0)
	s_barrier
	s_setprio 1
	s_waitcnt lgkmcnt(0)
	v_mfma_f32_16x16x32_bf16 v[126:129], v[132:135], v[182:185], v[126:129]
	v_mfma_f32_16x16x32_bf16 v[122:125], v[140:143], v[182:185], v[122:125]
	v_mfma_f32_16x16x32_bf16 v[118:121], v[132:135], v[192:195], v[118:121]
	v_mfma_f32_16x16x32_bf16 v[110:113], v[140:143], v[192:195], v[110:113]
	v_mfma_f32_16x16x32_bf16 v[102:105], v[132:135], v[200:203], v[102:105]
	v_mfma_f32_16x16x32_bf16 v[94:97], v[140:143], v[200:203], v[94:97]
	v_mfma_f32_16x16x32_bf16 v[86:89], v[132:135], v[218:221], v[86:89]
	v_mfma_f32_16x16x32_bf16 v[78:81], v[140:143], v[218:221], v[78:81]
	v_mfma_f32_16x16x32_bf16 v[126:129], v[136:139], v[188:191], v[126:129]
	v_mfma_f32_16x16x32_bf16 v[122:125], v[144:147], v[188:191], v[122:125]
	v_mfma_f32_16x16x32_bf16 v[118:121], v[136:139], v[196:199], v[118:121]
	v_mfma_f32_16x16x32_bf16 v[110:113], v[144:147], v[196:199], v[110:113]
	v_mfma_f32_16x16x32_bf16 v[102:105], v[136:139], v[204:207], v[102:105]
	v_mfma_f32_16x16x32_bf16 v[94:97], v[144:147], v[204:207], v[94:97]
	v_mfma_f32_16x16x32_bf16 v[86:89], v[136:139], v[222:225], v[86:89]
	v_mfma_f32_16x16x32_bf16 v[78:81], v[144:147], v[222:225], v[78:81]
	s_setprio 0
	s_setprio 1
	v_mfma_f32_16x16x32_bf16 v[114:117], v[148:151], v[182:185], v[114:117]
	v_mfma_f32_16x16x32_bf16 v[106:109], v[156:159], v[182:185], v[106:109]
	v_mfma_f32_16x16x32_bf16 v[98:101], v[148:151], v[192:195], v[98:101]
	v_mfma_f32_16x16x32_bf16 v[90:93], v[156:159], v[192:195], v[90:93]
	v_mfma_f32_16x16x32_bf16 v[82:85], v[148:151], v[200:203], v[82:85]
	v_mfma_f32_16x16x32_bf16 v[74:77], v[156:159], v[200:203], v[74:77]
	v_mfma_f32_16x16x32_bf16 v[70:73], v[148:151], v[218:221], v[70:73]
	v_mfma_f32_16x16x32_bf16 v[66:69], v[156:159], v[218:221], v[66:69]
	v_mfma_f32_16x16x32_bf16 v[114:117], v[152:155], v[188:191], v[114:117]
	v_mfma_f32_16x16x32_bf16 v[106:109], v[178:181], v[188:191], v[106:109]
	v_mfma_f32_16x16x32_bf16 v[98:101], v[152:155], v[196:199], v[98:101]
	v_mfma_f32_16x16x32_bf16 v[90:93], v[178:181], v[196:199], v[90:93]
	v_mfma_f32_16x16x32_bf16 v[82:85], v[152:155], v[204:207], v[82:85]
	v_mfma_f32_16x16x32_bf16 v[74:77], v[178:181], v[204:207], v[74:77]
	v_mfma_f32_16x16x32_bf16 v[70:73], v[152:155], v[222:225], v[70:73]
	v_mfma_f32_16x16x32_bf16 v[66:69], v[178:181], v[222:225], v[66:69]
	s_setprio 0
	s_barrier
; #define PG8_STAGE(bufoff, gbase, voff) do { _Pragma("unroll") for (int _i = 0; _i < 2; ++_i) \
;         __builtin_amdgcn_global_load_lds((const unsigned*)((const char*)(gbase) + (voff)[_i]), (PG8_LAS unsigned*)(lds + (bufoff) + ldsw + _i * 8192), 16, 0, 0); } while (0)
; #define PG8_LDA(dst, b, h) do { _Pragma("unroll") for (int m = 0; m < 4; ++m) _Pragma("unroll") for (int k = 0; k < 2; ++k) dst[m][k] = *(const PG8_LAS bf16x8*)(lds + PG8_SA(b, h) + aoff + m * 2048 + k * 1024); } while (0)
; #define PG8_MMA(ai, bj, At, Bt) do { __builtin_amdgcn_s_setprio(1); _Pragma("unroll") for (int m = 0; m < 4; ++m) _Pragma("unroll") for (int n = 0; n < 2; ++n) _Pragma("unroll") for (int k = 0; k < 2; ++k) \
;         acc[ai][bj][m][n] = __builtin_amdgcn_mfma_f32_16x16x32_bf16(Bt[n][k], At[m][k], acc[ai][bj][m][n], 0, 0, 0); __builtin_amdgcn_s_setprio(0); } while (0)
; #define PG8_WAIT_V(n) asm volatile("s_waitcnt vmcnt(" #n ")" ::: "memory")
; #define PG8_WAIT_L(n) asm volatile("s_waitcnt lgkmcnt(" #n ")" ::: "memory")
; #define PG8_BAR __builtin_amdgcn_s_barrier()
; #define PG8_SCHED __builtin_amdgcn_sched_barrier(0)
; #define PG8_STAGE(bufoff, gbase, voff) do { _Pragma("unroll") for (int _i = 0; _i < 2; ++_i) \
;         __builtin_amdgcn_global_load_lds((const unsigned*)((const char*)(gbase) + (voff)[_i]), (PG8_LAS unsigned*)(lds + (bufoff) + ldsw + _i * 8192), 16, 0, 0); } while (0)
; #define PG8_LDA(dst, b, h) do { _Pragma("unroll") for (int m = 0; m < 4; ++m) _Pragma("unroll") for (int k = 0; k < 2; ++k) dst[m][k] = *(const PG8_LAS bf16x8*)(lds + PG8_SA(b, h) + aoff + m * 2048 + k * 1024); } while (0)
; #define PG8_WAIT_V(n) asm volatile("s_waitcnt vmcnt(" #n ")" ::: "memory")
; template <class Epi, class Sched, bool ALIGN_EPI = false, bool SP2 = false>
; __device__ __forceinline__ void gemm_phase(PG8_LAS unsigned char* lds, const Gemm g, const Sched& S, const Epi& E) {
;     ...
;             PG8_LDA(At, 1, 1); PG8_STAGE(PG8_SB(1, 0), b3, voffB); PG8_STAGE(PG8_SB(1, 1), b3 + hstep, voffB); PG8_STAGE(PG8_SA(1, 0), a3, voffA);
;             PG8_WAIT_V(8); PG8_WAIT_L(0); PG8_BAR; PG8_MMA(1, 0, At, B0); PG8_MMA(1, 1, At, B1); PG8_BAR; PG8_SCHED;
;     ...
;         if constexpr (Sched::DYNAMIC) { static_assert(!Sched::DYNAMIC || ALIGN_EPI, "dynamic orders publish in front of the ALIGN_EPI barrier"); S.claim_publish(ui + 2, pend, wid, lane); }
	s_setprio 2
	s_add_i32 s4, s96, s66
	v_lshl_add_u64 v[160:161], v[160:161], 0, s[40:41]
	s_mov_b32 m0, s4
	ds_read_b128 v[182:185], v215 offset:49152
	ds_read_b128 v[188:191], v215 offset:50176
	ds_read_b128 v[192:195], v215 offset:51200
	ds_read_b128 v[196:199], v215 offset:52224
	ds_read_b128 v[200:203], v215 offset:53248
	ds_read_b128 v[204:207], v215 offset:54272
	ds_read_b128 v[218:221], v215 offset:55296
	ds_read_b128 v[222:225], v215 offset:56320
	global_load_lds_dwordx4 v[160:161], off
	s_add_i32 m0, s4, 0x2000
	s_add_u32 s2, s2, 0x80080
	v_lshl_add_u64 v[160:161], v[208:209], 0, s[40:41]
	s_addc_u32 s3, s3, 0
	s_add_i32 s4, s97, s66
	global_load_lds_dwordx4 v[160:161], off
	v_lshl_add_u64 v[160:161], s[2:3], 0, v[164:165]
	s_mov_b32 m0, s4
	s_nop 0
	global_load_lds_dwordx4 v[160:161], off
	v_lshl_add_u64 v[160:161], s[2:3], 0, v[168:169]
	s_add_i32 m0, s4, 0x2000
	s_nop 0
	global_load_lds_dwordx4 v[160:161], off
	v_lshl_add_u64 v[160:161], v[226:227], 0, s[40:41]
	s_mov_b32 m0, s74
	s_nop 0
	global_load_lds_dwordx4 v[160:161], off
	v_lshl_add_u64 v[160:161], v[228:229], 0, s[40:41]
	s_mov_b32 m0, s75
	s_nop 0
	global_load_lds_dwordx4 v[160:161], off
	s_setprio 0
	s_waitcnt vmcnt(8)
	s_waitcnt lgkmcnt(0)
	s_barrier
	s_setprio 1
	s_waitcnt lgkmcnt(0)
	v_mfma_f32_16x16x32_bf16 v[62:65], v[132:135], v[182:185], v[62:65]
	v_mfma_f32_16x16x32_bf16 v[58:61], v[140:143], v[182:185], v[58:61]
	v_mfma_f32_16x16x32_bf16 v[54:57], v[132:135], v[192:195], v[54:57]
	v_mfma_f32_16x16x32_bf16 v[46:49], v[140:143], v[192:195], v[46:49]
	v_mfma_f32_16x16x32_bf16 v[38:41], v[132:135], v[200:203], v[38:41]
	v_mfma_f32_16x16x32_bf16 v[30:33], v[140:143], v[200:203], v[30:33]
	v_mfma_f32_16x16x32_bf16 v[22:25], v[132:135], v[218:221], v[22:25]
	v_mfma_f32_16x16x32_bf16 v[14:17], v[140:143], v[218:221], v[14:17]
	v_mfma_f32_16x16x32_bf16 v[62:65], v[136:139], v[188:191], v[62:65]
	v_mfma_f32_16x16x32_bf16 v[58:61], v[144:147], v[188:191], v[58:61]
	v_mfma_f32_16x16x32_bf16 v[54:57], v[136:139], v[196:199], v[54:57]
	v_mfma_f32_16x16x32_bf16 v[46:49], v[144:147], v[196:199], v[46:49]
	v_mfma_f32_16x16x32_bf16 v[38:41], v[136:139], v[204:207], v[38:41]
	v_mfma_f32_16x16x32_bf16 v[30:33], v[144:147], v[204:207], v[30:33]
	v_mfma_f32_16x16x32_bf16 v[22:25], v[136:139], v[222:225], v[22:25]
	v_mfma_f32_16x16x32_bf16 v[14:17], v[144:147], v[222:225], v[14:17]
	s_setprio 0
	s_setprio 1
	v_mfma_f32_16x16x32_bf16 v[50:53], v[148:151], v[182:185], v[50:53]
	v_mfma_f32_16x16x32_bf16 v[42:45], v[156:159], v[182:185], v[42:45]
	v_mfma_f32_16x16x32_bf16 v[34:37], v[148:151], v[192:195], v[34:37]
	v_mfma_f32_16x16x32_bf16 v[26:29], v[156:159], v[192:195], v[26:29]
	v_mfma_f32_16x16x32_bf16 v[18:21], v[148:151], v[200:203], v[18:21]
	v_mfma_f32_16x16x32_bf16 v[10:13], v[156:159], v[200:203], v[10:13]
	v_mfma_f32_16x16x32_bf16 v[6:9], v[148:151], v[218:221], v[6:9]
	v_mfma_f32_16x16x32_bf16 v[2:5], v[156:159], v[218:221], v[2:5]
	v_mfma_f32_16x16x32_bf16 v[50:53], v[152:155], v[188:191], v[50:53]
	v_mfma_f32_16x16x32_bf16 v[42:45], v[178:181], v[188:191], v[42:45]
	v_mfma_f32_16x16x32_bf16 v[34:37], v[152:155], v[196:199], v[34:37]
	v_mfma_f32_16x16x32_bf16 v[26:29], v[178:181], v[196:199], v[26:29]
	v_mfma_f32_16x16x32_bf16 v[18:21], v[152:155], v[204:207], v[18:21]
	v_mfma_f32_16x16x32_bf16 v[10:13], v[178:181], v[204:207], v[10:13]
	v_mfma_f32_16x16x32_bf16 v[6:9], v[152:155], v[222:225], v[6:9]
	v_mfma_f32_16x16x32_bf16 v[2:5], v[178:181], v[222:225], v[2:5]
	s_setprio 0
	s_barrier
	s_setprio 2
	s_add_i32 s95, s95, 2
	s_add_u32 s0, s0, 0x100
	s_addc_u32 s1, s1, 0
	s_add_u32 s84, s84, 0x100
	s_addc_u32 s85, s85, 0
	s_cmp_gt_u32 s95, 29
	s_cbranch_scc0 .LBB0_332
	s_waitcnt vmcnt(0)
	v_readfirstlane_b32 s2, v130
	s_and_saveexec_b64 s[0:1], s[10:11]
	s_cbranch_execz .LBB0_335
	s_and_b32 s3, s6, 3
	s_xor_b32 s3, s3, 2
	s_and_b64 s[4:5], s[42:43], exec
	s_cselect_b32 s3, s3, s76
	s_lshl_b32 s3, s3, 2
	s_add_i32 s3, s3, 0
	s_add_i32 s3, s3, 0x27da0
	v_mov_b32_e32 v130, s3
	v_mov_b32_e32 v131, s2
	ds_write_b32 v130, v131

; #define PG8_STAGE(bufoff, gbase, voff) do { _Pragma("unroll") for (int _i = 0; _i < 2; ++_i) \
;         __builtin_amdgcn_global_load_lds((const unsigned*)((const char*)(gbase) + (voff)[_i]), (PG8_LAS unsigned*)(lds + (bufoff) + ldsw + _i * 8192), 16, 0, 0); } while (0)
; #define PG8_LDA(dst, b, h) do { _Pragma("unroll") for (int m = 0; m < 4; ++m) _Pragma("unroll") for (int k = 0; k < 2; ++k) dst[m][k] = *(const PG8_LAS bf16x8*)(lds + PG8_SA(b, h) + aoff + m * 2048 + k * 1024); } while (0)
; #define PG8_LDB(dst, b, h) do { _Pragma("unroll") for (int n = 0; n < 2; ++n) _Pragma("unroll") for (int k = 0; k < 2; ++k) dst[n][k] = *(const PG8_LAS bf16x8*)(lds + PG8_SB(b, h) + boff + n * 2048 + k * 1024); } while (0)
; #define PG8_MMA(ai, bj, At, Bt) do { __builtin_amdgcn_s_setprio(1); _Pragma("unroll") for (int m = 0; m < 4; ++m) _Pragma("unroll") for (int n = 0; n < 2; ++n) _Pragma("unroll") for (int k = 0; k < 2; ++k) \
;         acc[ai][bj][m][n] = __builtin_amdgcn_mfma_f32_16x16x32_bf16(Bt[n][k], At[m][k], acc[ai][bj][m][n], 0, 0, 0); __builtin_amdgcn_s_setprio(0); } while (0)
; #define PG8_WAIT_V(n) asm volatile("s_waitcnt vmcnt(" #n ")" ::: "memory")
; #define PG8_WAIT_L(n) asm volatile("s_waitcnt lgkmcnt(" #n ")" ::: "memory")
; #define PG8_BAR __builtin_amdgcn_s_barrier()
; template <class Epi, class Sched, bool ALIGN_EPI = false, bool SP2 = false>
; __device__ __forceinline__ void gemm_phase(PG8_LAS unsigned char* lds, const Gemm g, const Sched& S, const Epi& E) {
;     ...
;             const char* a1 = cA + (size_t)(t + 1) * kstep;
;             const char* a2 = last ? nA : cA + (size_t)(t + 2) * kstep; const char* b2 = last ? nB : cB + (size_t)(t + 2) * kstep;
;             const char* a3 = a2 + kstep; const char* b3 = b2 + kstep;
;             if (last && has_next) S.a_ready(nxt);
;             if constexpr (SP2) {
;             PG8_LDB(B0, 0, 0); PG8_LDB(B1, 0, 1); PG8_SCHED; PG8_LDA(At, 0, 0); PG8_STAGE(PG8_SA(1, 1), a1 + hstep, voffA);
;             PG8_WAIT_V(8); PG8_WAIT_L(0); PG8_BAR; PG8_MMA(0, 0, At, B0); PG8_MMA(0, 1, At, B1); PG8_BAR; PG8_SCHED;
;             PG8_LDA(At, 0, 1); PG8_STAGE(PG8_SB(0, 0), b2, voffB); PG8_STAGE(PG8_SB(0, 1), b2 + hstep, voffB); PG8_STAGE(PG8_SA(0, 0), a2, voffA);
;             PG8_WAIT_V(8); PG8_WAIT_L(0); PG8_BAR; PG8_MMA(1, 0, At, B0); PG8_MMA(1, 1, At, B1); PG8_BAR; PG8_SCHED;
.LBB0_900:
	s_setprio 2
	ds_read_b128 v[114:117], v218
	ds_read_b128 v[118:121], v218 offset:1024
	ds_read_b128 v[138:141], v218 offset:2048
	ds_read_b128 v[142:145], v218 offset:3072
	ds_read_b128 v[146:149], v219
	ds_read_b128 v[150:153], v219 offset:1024
	ds_read_b128 v[154:157], v219 offset:2048
	ds_read_b128 v[158:161], v219 offset:3072
	s_add_u32 s34, s8, 0xfff80080
	s_addc_u32 s35, s9, -1
	s_cmp_eq_u32 s60, 28
	s_cselect_b32 s37, s19, s35
	s_cselect_b32 s36, s56, s34
	s_cselect_b32 s35, s17, s59
	s_cselect_b32 s34, s57, s58
	v_lshl_add_u64 v[170:171], s[8:9], 0, v[180:181]
	s_add_i32 m0, s27, 0xc000
	ds_read_b128 v[162:165], v220
	ds_read_b128 v[166:169], v220 offset:1024
	ds_read_b128 v[190:193], v220 offset:2048
	ds_read_b128 v[194:197], v220 offset:3072
	ds_read_b128 v[198:201], v220 offset:4096
	ds_read_b128 v[202:205], v220 offset:5120
	ds_read_b128 v[206:209], v220 offset:6144
	ds_read_b128 v[210:213], v220 offset:7168
	global_load_lds_dwordx4 v[170:171], off
	v_lshl_add_u64 v[170:171], s[8:9], 0, v[182:183]
	s_add_i32 m0, s27, 0xe000
	s_nop 0
	global_load_lds_dwordx4 v[170:171], off
	s_setprio 0
	s_waitcnt vmcnt(8)
	s_waitcnt lgkmcnt(0)
	s_barrier
	s_setprio 1
	s_waitcnt lgkmcnt(0)
	v_mfma_f32_16x16x32_bf16 v[134:137], v[114:117], v[162:165], v[134:137]
	v_mfma_f32_16x16x32_bf16 v[130:133], v[138:141], v[162:165], v[130:133]
	v_mfma_f32_16x16x32_bf16 v[126:129], v[114:117], v[190:193], v[126:129]
	v_mfma_f32_16x16x32_bf16 v[122:125], v[138:141], v[190:193], v[122:125]
	v_mfma_f32_16x16x32_bf16 v[110:113], v[114:117], v[198:201], v[110:113]
	v_mfma_f32_16x16x32_bf16 v[106:109], v[138:141], v[198:201], v[106:109]
	v_mfma_f32_16x16x32_bf16 v[102:105], v[114:117], v[206:209], v[102:105]
	v_mfma_f32_16x16x32_bf16 v[98:101], v[138:141], v[206:209], v[98:101]
	v_mfma_f32_16x16x32_bf16 v[134:137], v[118:121], v[166:169], v[134:137]
	v_mfma_f32_16x16x32_bf16 v[130:133], v[142:145], v[166:169], v[130:133]
	v_mfma_f32_16x16x32_bf16 v[126:129], v[118:121], v[194:197], v[126:129]
	v_mfma_f32_16x16x32_bf16 v[122:125], v[142:145], v[194:197], v[122:125]
	v_mfma_f32_16x16x32_bf16 v[110:113], v[118:121], v[202:205], v[110:113]
	v_mfma_f32_16x16x32_bf16 v[106:109], v[142:145], v[202:205], v[106:109]
	v_mfma_f32_16x16x32_bf16 v[102:105], v[118:121], v[210:213], v[102:105]
	v_mfma_f32_16x16x32_bf16 v[98:101], v[142:145], v[210:213], v[98:101]
	s_setprio 0
	s_setprio 1
	v_mfma_f32_16x16x32_bf16 v[62:65], v[146:149], v[162:165], v[62:65]
	v_mfma_f32_16x16x32_bf16 v[58:61], v[154:157], v[162:165], v[58:61]
	v_mfma_f32_16x16x32_bf16 v[54:57], v[146:149], v[190:193], v[54:57]
	v_mfma_f32_16x16x32_bf16 v[50:53], v[154:157], v[190:193], v[50:53]
	v_mfma_f32_16x16x32_bf16 v[46:49], v[146:149], v[198:201], v[46:49]
	v_mfma_f32_16x16x32_bf16 v[42:45], v[154:157], v[198:201], v[42:45]
	v_mfma_f32_16x16x32_bf16 v[38:41], v[146:149], v[206:209], v[38:41]
	v_mfma_f32_16x16x32_bf16 v[34:37], v[154:157], v[206:209], v[34:37]
	v_mfma_f32_16x16x32_bf16 v[62:65], v[150:153], v[166:169], v[62:65]
	v_mfma_f32_16x16x32_bf16 v[58:61], v[158:161], v[166:169], v[58:61]
	v_mfma_f32_16x16x32_bf16 v[54:57], v[150:153], v[194:197], v[54:57]
	v_mfma_f32_16x16x32_bf16 v[50:53], v[158:161], v[194:197], v[50:53]
	v_mfma_f32_16x16x32_bf16 v[46:49], v[150:153], v[202:205], v[46:49]
	v_mfma_f32_16x16x32_bf16 v[42:45], v[158:161], v[202:205], v[42:45]
	v_mfma_f32_16x16x32_bf16 v[38:41], v[150:153], v[210:213], v[38:41]
	v_mfma_f32_16x16x32_bf16 v[34:37], v[158:161], v[210:213], v[34:37]
	s_setprio 0
	s_barrier
	s_setprio 2
	s_add_i32 s61, s54, s40
	v_lshl_add_u64 v[170:171], s[34:35], 0, v[174:175]
	s_mov_b32 m0, s61
	ds_read_b128 v[162:165], v220 offset:16384
	ds_read_b128 v[166:169], v220 offset:17408
	ds_read_b128 v[190:193], v220 offset:18432
	ds_read_b128 v[194:197], v220 offset:19456
	ds_read_b128 v[198:201], v220 offset:20480
	ds_read_b128 v[202:205], v220 offset:21504
	ds_read_b128 v[206:209], v220 offset:22528
	ds_read_b128 v[210:213], v220 offset:23552
	global_load_lds_dwordx4 v[170:171], off
	s_add_i32 m0, s61, 0x2000
	s_add_u32 s62, s34, 0x80000
	v_lshl_add_u64 v[214:215], s[34:35], 0, v[178:179]
	s_addc_u32 s63, s35, 0
	s_add_i32 s61, s55, s40
	global_load_lds_dwordx4 v[214:215], off
	v_lshl_add_u64 v[222:223], s[62:63], 0, v[174:175]
	s_mov_b32 m0, s61
	v_lshl_add_u64 v[224:225], s[36:37], 0, v[176:177]
	global_load_lds_dwordx4 v[222:223], off
	v_lshl_add_u64 v[222:223], s[62:63], 0, v[178:179]
	s_add_i32 m0, s61, 0x2000
	s_nop 0
	global_load_lds_dwordx4 v[222:223], off
	v_lshl_add_u64 v[222:223], s[36:37], 0, v[172:173]
	s_mov_b32 m0, s27
	s_nop 0
	global_load_lds_dwordx4 v[222:223], off
	s_mov_b32 m0, s29
	s_nop 0
	global_load_lds_dwordx4 v[224:225], off
	s_setprio 0
	s_waitcnt vmcnt(8)
	s_waitcnt lgkmcnt(0)
	s_barrier
; #define PG8_STAGE(bufoff, gbase, voff) do { _Pragma("unroll") for (int _i = 0; _i < 2; ++_i) \
;         __builtin_amdgcn_global_load_lds((const unsigned*)((const char*)(gbase) + (voff)[_i]), (PG8_LAS unsigned*)(lds + (bufoff) + ldsw + _i * 8192), 16, 0, 0); } while (0)
; #define PG8_LDA(dst, b, h) do { _Pragma("unroll") for (int m = 0; m < 4; ++m) _Pragma("unroll") for (int k = 0; k < 2; ++k) dst[m][k] = *(const PG8_LAS bf16x8*)(lds + PG8_SA(b, h) + aoff + m * 2048 + k * 1024); } while (0)
; #define PG8_LDB(dst, b, h) do { _Pragma("unroll") for (int n = 0; n < 2; ++n) _Pragma("unroll") for (int k = 0; k < 2; ++k) dst[n][k] = *(const PG8_LAS bf16x8*)(lds + PG8_SB(b, h) + boff + n * 2048 + k * 1024); } while (0)
; #define PG8_MMA(ai, bj, At, Bt) do { __builtin_amdgcn_s_setprio(1); _Pragma("unroll") for (int m = 0; m < 4; ++m) _Pragma("unroll") for (int n = 0; n < 2; ++n) _Pragma("unroll") for (int k = 0; k < 2; ++k) \
;         acc[ai][bj][m][n] = __builtin_amdgcn_mfma_f32_16x16x32_bf16(Bt[n][k], At[m][k], acc[ai][bj][m][n], 0, 0, 0); __builtin_amdgcn_s_setprio(0); } while (0)
; #define PG8_WAIT_V(n) asm volatile("s_waitcnt vmcnt(" #n ")" ::: "memory")
; #define PG8_WAIT_L(n) asm volatile("s_waitcnt lgkmcnt(" #n ")" ::: "memory")
; #define PG8_BAR __builtin_amdgcn_s_barrier()
; #define PG8_SCHED __builtin_amdgcn_sched_barrier(0)
; #define PG8_STAGE(bufoff, gbase, voff) do { _Pragma("unroll") for (int _i = 0; _i < 2; ++_i) \
;         __builtin_amdgcn_global_load_lds((const unsigned*)((const char*)(gbase) + (voff)[_i]), (PG8_LAS unsigned*)(lds + (bufoff) + ldsw + _i * 8192), 16, 0, 0); } while (0)
; #define PG8_WAIT_V(n) asm volatile("s_waitcnt vmcnt(" #n ")" ::: "memory")
; #define PG8_WAIT_L(n) asm volatile("s_waitcnt lgkmcnt(" #n ")" ::: "memory")
; #define PG8_BAR __builtin_amdgcn_s_barrier()
; template <class Epi, class Sched, bool ALIGN_EPI = false, bool SP2 = false>
; __device__ __forceinline__ void gemm_phase(PG8_LAS unsigned char* lds, const Gemm g, const Sched& S, const Epi& E) {
;     ...
;             PG8_WAIT_V(8); PG8_WAIT_L(0); PG8_BAR; PG8_MMA(1, 0, At, B0); PG8_MMA(1, 1, At, B1); PG8_BAR; PG8_SCHED;
;             PG8_LDB(B0, 1, 0); PG8_LDB(B1, 1, 1); PG8_SCHED; PG8_LDA(At, 1, 0); PG8_STAGE(PG8_SA(0, 1), a2 + hstep, voffA);
;             PG8_WAIT_V(8); PG8_WAIT_L(0); PG8_BAR; PG8_MMA(0, 0, At, B0); PG8_MMA(0, 1, At, B1); PG8_BAR; PG8_SCHED;
	s_setprio 1
	s_waitcnt lgkmcnt(0)
	v_mfma_f32_16x16x32_bf16 v[94:97], v[114:117], v[162:165], v[94:97]
	v_mfma_f32_16x16x32_bf16 v[90:93], v[138:141], v[162:165], v[90:93]
	v_mfma_f32_16x16x32_bf16 v[86:89], v[114:117], v[190:193], v[86:89]
	v_mfma_f32_16x16x32_bf16 v[82:85], v[138:141], v[190:193], v[82:85]
	v_mfma_f32_16x16x32_bf16 v[78:81], v[114:117], v[198:201], v[78:81]
	v_mfma_f32_16x16x32_bf16 v[74:77], v[138:141], v[198:201], v[74:77]
	v_mfma_f32_16x16x32_bf16 v[70:73], v[114:117], v[206:209], v[70:73]
	v_mfma_f32_16x16x32_bf16 v[66:69], v[138:141], v[206:209], v[66:69]
	v_mfma_f32_16x16x32_bf16 v[94:97], v[118:121], v[166:169], v[94:97]
	v_mfma_f32_16x16x32_bf16 v[90:93], v[142:145], v[166:169], v[90:93]
	v_mfma_f32_16x16x32_bf16 v[86:89], v[118:121], v[194:197], v[86:89]
	v_mfma_f32_16x16x32_bf16 v[82:85], v[142:145], v[194:197], v[82:85]
	v_mfma_f32_16x16x32_bf16 v[78:81], v[118:121], v[202:205], v[78:81]
	v_mfma_f32_16x16x32_bf16 v[74:77], v[142:145], v[202:205], v[74:77]
	v_mfma_f32_16x16x32_bf16 v[70:73], v[118:121], v[210:213], v[70:73]
	v_mfma_f32_16x16x32_bf16 v[66:69], v[142:145], v[210:213], v[66:69]
	s_setprio 0
	s_setprio 1
	v_mfma_f32_16x16x32_bf16 v[30:33], v[146:149], v[162:165], v[30:33]
	v_mfma_f32_16x16x32_bf16 v[26:29], v[154:157], v[162:165], v[26:29]
	v_mfma_f32_16x16x32_bf16 v[22:25], v[146:149], v[190:193], v[22:25]
	v_mfma_f32_16x16x32_bf16 v[18:21], v[154:157], v[190:193], v[18:21]
	v_mfma_f32_16x16x32_bf16 v[14:17], v[146:149], v[198:201], v[14:17]
	v_mfma_f32_16x16x32_bf16 v[10:13], v[154:157], v[198:201], v[10:13]
	v_mfma_f32_16x16x32_bf16 v[6:9], v[146:149], v[206:209], v[6:9]
	v_mfma_f32_16x16x32_bf16 v[2:5], v[154:157], v[206:209], v[2:5]
	v_mfma_f32_16x16x32_bf16 v[30:33], v[150:153], v[166:169], v[30:33]
	v_mfma_f32_16x16x32_bf16 v[26:29], v[158:161], v[166:169], v[26:29]
	v_mfma_f32_16x16x32_bf16 v[22:25], v[150:153], v[194:197], v[22:25]
	v_mfma_f32_16x16x32_bf16 v[18:21], v[158:161], v[194:197], v[18:21]
	v_mfma_f32_16x16x32_bf16 v[14:17], v[150:153], v[202:205], v[14:17]
	v_mfma_f32_16x16x32_bf16 v[10:13], v[158:161], v[202:205], v[10:13]
	v_mfma_f32_16x16x32_bf16 v[6:9], v[150:153], v[210:213], v[6:9]
	v_mfma_f32_16x16x32_bf16 v[2:5], v[158:161], v[210:213], v[2:5]
	s_setprio 0
	s_barrier
	s_setprio 2
	s_add_i32 s61, 0, 0x18000
	s_add_i32 s62, 0, 0x1c000
	v_add_u32_e32 v142, s61, v217
	v_add_u32_e32 v158, s62, v217
	ds_read_b128 v[114:117], v142
	ds_read_b128 v[118:121], v142 offset:1024
	ds_read_b128 v[138:141], v142 offset:2048
	ds_read_b128 v[142:145], v142 offset:3072
	ds_read_b128 v[146:149], v158
	ds_read_b128 v[150:153], v158 offset:1024
	ds_read_b128 v[154:157], v158 offset:2048
	ds_read_b128 v[158:161], v158 offset:3072
	s_add_u32 s36, s36, 0x80000
	s_addc_u32 s37, s37, 0
	s_mov_b32 m0, s41
	v_lshl_add_u64 v[226:227], s[36:37], 0, v[172:173]
	ds_read_b128 v[162:165], v220 offset:32768
	ds_read_b128 v[166:169], v220 offset:33792
	ds_read_b128 v[190:193], v220 offset:34816
	ds_read_b128 v[194:197], v220 offset:35840
	ds_read_b128 v[198:201], v220 offset:36864
	ds_read_b128 v[202:205], v220 offset:37888
	ds_read_b128 v[206:209], v220 offset:38912
	ds_read_b128 v[210:213], v220 offset:39936
	global_load_lds_dwordx4 v[226:227], off
	v_lshl_add_u64 v[226:227], s[36:37], 0, v[176:177]
	s_mov_b32 m0, s42
	s_nop 0
	global_load_lds_dwordx4 v[226:227], off
	s_setprio 0
	s_waitcnt vmcnt(8)
	s_waitcnt lgkmcnt(0)
	s_barrier
	s_setprio 1
	s_waitcnt lgkmcnt(0)
	v_mfma_f32_16x16x32_bf16 v[134:137], v[114:117], v[162:165], v[134:137]
	v_mfma_f32_16x16x32_bf16 v[130:133], v[138:141], v[162:165], v[130:133]
	v_mfma_f32_16x16x32_bf16 v[126:129], v[114:117], v[190:193], v[126:129]
	v_mfma_f32_16x16x32_bf16 v[122:125], v[138:141], v[190:193], v[122:125]
	v_mfma_f32_16x16x32_bf16 v[110:113], v[114:117], v[198:201], v[110:113]
	v_mfma_f32_16x16x32_bf16 v[106:109], v[138:141], v[198:201], v[106:109]
	v_mfma_f32_16x16x32_bf16 v[102:105], v[114:117], v[206:209], v[102:105]
	v_mfma_f32_16x16x32_bf16 v[98:101], v[138:141], v[206:209], v[98:101]
	v_mfma_f32_16x16x32_bf16 v[134:137], v[118:121], v[166:169], v[134:137]
	v_mfma_f32_16x16x32_bf16 v[130:133], v[142:145], v[166:169], v[130:133]
	v_mfma_f32_16x16x32_bf16 v[126:129], v[118:121], v[194:197], v[126:129]
	v_mfma_f32_16x16x32_bf16 v[122:125], v[142:145], v[194:197], v[122:125]
	v_mfma_f32_16x16x32_bf16 v[110:113], v[118:121], v[202:205], v[110:113]
	v_mfma_f32_16x16x32_bf16 v[106:109], v[142:145], v[202:205], v[106:109]
	v_mfma_f32_16x16x32_bf16 v[102:105], v[118:121], v[210:213], v[102:105]
	v_mfma_f32_16x16x32_bf16 v[98:101], v[142:145], v[210:213], v[98:101]
	s_setprio 0
	s_setprio 1
	v_mfma_f32_16x16x32_bf16 v[62:65], v[146:149], v[162:165], v[62:65]
	v_mfma_f32_16x16x32_bf16 v[58:61], v[154:157], v[162:165], v[58:61]
	v_mfma_f32_16x16x32_bf16 v[54:57], v[146:149], v[190:193], v[54:57]
	v_mfma_f32_16x16x32_bf16 v[50:53], v[154:157], v[190:193], v[50:53]
	v_mfma_f32_16x16x32_bf16 v[46:49], v[146:149], v[198:201], v[46:49]
	v_mfma_f32_16x16x32_bf16 v[42:45], v[154:157], v[198:201], v[42:45]
	v_mfma_f32_16x16x32_bf16 v[38:41], v[146:149], v[206:209], v[38:41]
	v_mfma_f32_16x16x32_bf16 v[34:37], v[154:157], v[206:209], v[34:37]
	v_mfma_f32_16x16x32_bf16 v[62:65], v[150:153], v[166:169], v[62:65]
	v_mfma_f32_16x16x32_bf16 v[58:61], v[158:161], v[166:169], v[58:61]
	v_mfma_f32_16x16x32_bf16 v[54:57], v[150:153], v[194:197], v[54:57]
	v_mfma_f32_16x16x32_bf16 v[50:53], v[158:161], v[194:197], v[50:53]
	v_mfma_f32_16x16x32_bf16 v[46:49], v[150:153], v[202:205], v[46:49]
	v_mfma_f32_16x16x32_bf16 v[42:45], v[158:161], v[202:205], v[42:45]
	v_mfma_f32_16x16x32_bf16 v[38:41], v[150:153], v[210:213], v[38:41]
	v_mfma_f32_16x16x32_bf16 v[34:37], v[158:161], v[210:213], v[34:37]
	s_setprio 0
	s_barrier
; #define PG8_STAGE(bufoff, gbase, voff) do { _Pragma("unroll") for (int _i = 0; _i < 2; ++_i) \
;         __builtin_amdgcn_global_load_lds((const unsigned*)((const char*)(gbase) + (voff)[_i]), (PG8_LAS unsigned*)(lds + (bufoff) + ldsw + _i * 8192), 16, 0, 0); } while (0)
; #define PG8_LDA(dst, b, h) do { _Pragma("unroll") for (int m = 0; m < 4; ++m) _Pragma("unroll") for (int k = 0; k < 2; ++k) dst[m][k] = *(const PG8_LAS bf16x8*)(lds + PG8_SA(b, h) + aoff + m * 2048 + k * 1024); } while (0)
; #define PG8_MMA(ai, bj, At, Bt) do { __builtin_amdgcn_s_setprio(1); _Pragma("unroll") for (int m = 0; m < 4; ++m) _Pragma("unroll") for (int n = 0; n < 2; ++n) _Pragma("unroll") for (int k = 0; k < 2; ++k) \
;         acc[ai][bj][m][n] = __builtin_amdgcn_mfma_f32_16x16x32_bf16(Bt[n][k], At[m][k], acc[ai][bj][m][n], 0, 0, 0); __builtin_amdgcn_s_setprio(0); } while (0)
; #define PG8_WAIT_V(n) asm volatile("s_waitcnt vmcnt(" #n ")" ::: "memory")
; #define PG8_WAIT_L(n) asm volatile("s_waitcnt lgkmcnt(" #n ")" ::: "memory")
; #define PG8_BAR __builtin_amdgcn_s_barrier()
; #define PG8_SCHED __builtin_amdgcn_sched_barrier(0)
; #define PG8_STAGE(bufoff, gbase, voff) do { _Pragma("unroll") for (int _i = 0; _i < 2; ++_i) \
;         __builtin_amdgcn_global_load_lds((const unsigned*)((const char*)(gbase) + (voff)[_i]), (PG8_LAS unsigned*)(lds + (bufoff) + ldsw + _i * 8192), 16, 0, 0); } while (0)
; #define PG8_LDA(dst, b, h) do { _Pragma("unroll") for (int m = 0; m < 4; ++m) _Pragma("unroll") for (int k = 0; k < 2; ++k) dst[m][k] = *(const PG8_LAS bf16x8*)(lds + PG8_SA(b, h) + aoff + m * 2048 + k * 1024); } while (0)
; #define PG8_WAIT_V(n) asm volatile("s_waitcnt vmcnt(" #n ")" ::: "memory")
; #define PG8_WAIT_L(n) asm volatile("s_waitcnt lgkmcnt(" #n ")" ::: "memory")
; #define PG8_BAR __builtin_amdgcn_s_barrier()
; template <class Epi, class Sched, bool ALIGN_EPI = false, bool SP2 = false>
; __device__ __forceinline__ void gemm_phase(PG8_LAS unsigned char* lds, const Gemm g, const Sched& S, const Epi& E) {
;     ...
;             PG8_LDA(At, 1, 1); PG8_STAGE(PG8_SB(1, 0), b3, voffB); PG8_STAGE(PG8_SB(1, 1), b3 + hstep, voffB); PG8_STAGE(PG8_SA(1, 0), a3, voffA);
;             PG8_WAIT_V(8); PG8_WAIT_L(0); PG8_BAR; PG8_MMA(1, 0, At, B0); PG8_MMA(1, 1, At, B1); PG8_BAR; PG8_SCHED;
;     ...
;         if constexpr (ALIGN_EPI) { if (wr == 0) PG8_BAR; }
	s_setprio 2
	s_add_i32 s36, s61, s40
	v_lshl_add_u64 v[170:171], v[170:171], 0, s[10:11]
	s_mov_b32 m0, s36
	ds_read_b128 v[162:165], v220 offset:49152
	ds_read_b128 v[166:169], v220 offset:50176
	ds_read_b128 v[190:193], v220 offset:51200
	ds_read_b128 v[194:197], v220 offset:52224
	ds_read_b128 v[198:201], v220 offset:53248
	ds_read_b128 v[202:205], v220 offset:54272
	ds_read_b128 v[206:209], v220 offset:55296
	ds_read_b128 v[210:213], v220 offset:56320
	global_load_lds_dwordx4 v[170:171], off
	s_add_i32 m0, s36, 0x2000
	s_add_u32 s34, s34, 0x80080
	v_lshl_add_u64 v[170:171], v[214:215], 0, s[10:11]
	s_addc_u32 s35, s35, 0
	s_add_i32 s36, s62, s40
	global_load_lds_dwordx4 v[170:171], off
	v_lshl_add_u64 v[170:171], s[34:35], 0, v[174:175]
	s_mov_b32 m0, s36
	s_nop 0
	global_load_lds_dwordx4 v[170:171], off
	v_lshl_add_u64 v[170:171], s[34:35], 0, v[178:179]
	s_add_i32 m0, s36, 0x2000
	s_nop 0
	global_load_lds_dwordx4 v[170:171], off
	v_lshl_add_u64 v[170:171], v[222:223], 0, s[10:11]
	s_mov_b32 m0, s51
	s_nop 0
	global_load_lds_dwordx4 v[170:171], off
	v_lshl_add_u64 v[170:171], v[224:225], 0, s[10:11]
	s_mov_b32 m0, s52
	s_nop 0
	global_load_lds_dwordx4 v[170:171], off
	s_setprio 0
	s_waitcnt vmcnt(8)
	s_waitcnt lgkmcnt(0)
	s_barrier
	s_setprio 1
	s_waitcnt lgkmcnt(0)
	v_mfma_f32_16x16x32_bf16 v[94:97], v[114:117], v[162:165], v[94:97]
	v_mfma_f32_16x16x32_bf16 v[90:93], v[138:141], v[162:165], v[90:93]
	v_mfma_f32_16x16x32_bf16 v[86:89], v[114:117], v[190:193], v[86:89]
	v_mfma_f32_16x16x32_bf16 v[82:85], v[138:141], v[190:193], v[82:85]
	v_mfma_f32_16x16x32_bf16 v[78:81], v[114:117], v[198:201], v[78:81]
	v_mfma_f32_16x16x32_bf16 v[74:77], v[138:141], v[198:201], v[74:77]
	v_mfma_f32_16x16x32_bf16 v[70:73], v[114:117], v[206:209], v[70:73]
	v_mfma_f32_16x16x32_bf16 v[66:69], v[138:141], v[206:209], v[66:69]
	v_mfma_f32_16x16x32_bf16 v[94:97], v[118:121], v[166:169], v[94:97]
	v_mfma_f32_16x16x32_bf16 v[90:93], v[142:145], v[166:169], v[90:93]
	v_mfma_f32_16x16x32_bf16 v[86:89], v[118:121], v[194:197], v[86:89]
	v_mfma_f32_16x16x32_bf16 v[82:85], v[142:145], v[194:197], v[82:85]
	v_mfma_f32_16x16x32_bf16 v[78:81], v[118:121], v[202:205], v[78:81]
	v_mfma_f32_16x16x32_bf16 v[74:77], v[142:145], v[202:205], v[74:77]
	v_mfma_f32_16x16x32_bf16 v[70:73], v[118:121], v[210:213], v[70:73]
	v_mfma_f32_16x16x32_bf16 v[66:69], v[142:145], v[210:213], v[66:69]
	s_setprio 0
	s_setprio 1
	v_mfma_f32_16x16x32_bf16 v[30:33], v[146:149], v[162:165], v[30:33]
	v_mfma_f32_16x16x32_bf16 v[26:29], v[154:157], v[162:165], v[26:29]
	v_mfma_f32_16x16x32_bf16 v[22:25], v[146:149], v[190:193], v[22:25]
	v_mfma_f32_16x16x32_bf16 v[18:21], v[154:157], v[190:193], v[18:21]
	v_mfma_f32_16x16x32_bf16 v[14:17], v[146:149], v[198:201], v[14:17]
	v_mfma_f32_16x16x32_bf16 v[10:13], v[154:157], v[198:201], v[10:13]
	v_mfma_f32_16x16x32_bf16 v[6:9], v[146:149], v[206:209], v[6:9]
	v_mfma_f32_16x16x32_bf16 v[2:5], v[154:157], v[206:209], v[2:5]
	v_mfma_f32_16x16x32_bf16 v[30:33], v[150:153], v[166:169], v[30:33]
	v_mfma_f32_16x16x32_bf16 v[26:29], v[158:161], v[166:169], v[26:29]
	v_mfma_f32_16x16x32_bf16 v[22:25], v[150:153], v[194:197], v[22:25]
	v_mfma_f32_16x16x32_bf16 v[18:21], v[158:161], v[194:197], v[18:21]
	v_mfma_f32_16x16x32_bf16 v[14:17], v[150:153], v[202:205], v[14:17]
	v_mfma_f32_16x16x32_bf16 v[10:13], v[158:161], v[202:205], v[10:13]
	v_mfma_f32_16x16x32_bf16 v[6:9], v[150:153], v[210:213], v[6:9]
	v_mfma_f32_16x16x32_bf16 v[2:5], v[158:161], v[210:213], v[2:5]
	s_setprio 0
	s_barrier
	s_setprio 2
	s_add_i32 s60, s60, 2
	s_add_u32 s8, s8, 0x100
	s_addc_u32 s9, s9, 0
	s_add_u32 s58, s58, 0x100
	s_addc_u32 s59, s59, 0
	s_cmp_gt_u32 s60, 29
	s_cbranch_scc0 .LBB0_900
	s_and_b64 vcc, exec, s[12:13]
	s_cbranch_vccz .LBB0_903
	s_barrier

; #define PG8_STAGE(bufoff, gbase, voff) do { _Pragma("unroll") for (int _i = 0; _i < 2; ++_i) \
;         __builtin_amdgcn_global_load_lds((const unsigned*)((const char*)(gbase) + (voff)[_i]), (PG8_LAS unsigned*)(lds + (bufoff) + ldsw + _i * 8192), 16, 0, 0); } while (0)
; #define PG8_LDA(dst, b, h) do { _Pragma("unroll") for (int m = 0; m < 4; ++m) _Pragma("unroll") for (int k = 0; k < 2; ++k) dst[m][k] = *(const PG8_LAS bf16x8*)(lds + PG8_SA(b, h) + aoff + m * 2048 + k * 1024); } while (0)
; #define PG8_LDB(dst, b, h) do { _Pragma("unroll") for (int n = 0; n < 2; ++n) _Pragma("unroll") for (int k = 0; k < 2; ++k) dst[n][k] = *(const PG8_LAS bf16x8*)(lds + PG8_SB(b, h) + boff + n * 2048 + k * 1024); } while (0)
; #define PG8_MMA(ai, bj, At, Bt) do { __builtin_amdgcn_s_setprio(1); _Pragma("unroll") for (int m = 0; m < 4; ++m) _Pragma("unroll") for (int n = 0; n < 2; ++n) _Pragma("unroll") for (int k = 0; k < 2; ++k) \
;         acc[ai][bj][m][n] = __builtin_amdgcn_mfma_f32_16x16x32_bf16(Bt[n][k], At[m][k], acc[ai][bj][m][n], 0, 0, 0); __builtin_amdgcn_s_setprio(0); } while (0)
; #define PG8_WAIT_V(n) asm volatile("s_waitcnt vmcnt(" #n ")" ::: "memory")
; #define PG8_WAIT_L(n) asm volatile("s_waitcnt lgkmcnt(" #n ")" ::: "memory")
; #define PG8_BAR __builtin_amdgcn_s_barrier()
; template <class Epi, class Sched, bool ALIGN_EPI = false, bool SP2 = false>
; __device__ __forceinline__ void gemm_phase(PG8_LAS unsigned char* lds, const Gemm g, const Sched& S, const Epi& E) {
;     ...
;             const char* a1 = cA + (size_t)(t + 1) * kstep;
;             const char* a2 = last ? nA : cA + (size_t)(t + 2) * kstep; const char* b2 = last ? nB : cB + (size_t)(t + 2) * kstep;
;             const char* a3 = a2 + kstep; const char* b3 = b2 + kstep;
;             if (last && has_next) S.a_ready(nxt);
;             if constexpr (SP2) {
;             PG8_LDB(B0, 0, 0); PG8_LDB(B1, 0, 1); PG8_SCHED; PG8_LDA(At, 0, 0); PG8_STAGE(PG8_SA(1, 1), a1 + hstep, voffA);
;             PG8_WAIT_V(8); PG8_WAIT_L(0); PG8_BAR; PG8_MMA(0, 0, At, B0); PG8_MMA(0, 1, At, B1); PG8_BAR; PG8_SCHED;
;             PG8_LDA(At, 0, 1); PG8_STAGE(PG8_SB(0, 0), b2, voffB); PG8_STAGE(PG8_SB(0, 1), b2 + hstep, voffB); PG8_STAGE(PG8_SA(0, 0), a2, voffA);
;             PG8_WAIT_V(8); PG8_WAIT_L(0); PG8_BAR; PG8_MMA(1, 0, At, B0); PG8_MMA(1, 1, At, B1); PG8_BAR; PG8_SCHED;
.LBB0_1011:
	s_setprio 2
	ds_read_b128 v[154:157], v150
	ds_read_b128 v[158:161], v150 offset:1024
	ds_read_b128 v[162:165], v150 offset:2048
	ds_read_b128 v[166:169], v150 offset:3072
	ds_read_b128 v[170:173], v151
	ds_read_b128 v[174:177], v151 offset:1024
	ds_read_b128 v[178:181], v151 offset:2048
	ds_read_b128 v[182:185], v151 offset:3072
	s_add_u32 s34, s30, 0xfff80080
	s_addc_u32 s35, s31, -1
	s_cmp_eq_u32 s57, 28
	s_cselect_b32 s37, s23, s35
	s_cselect_b32 s36, s53, s34
	s_cselect_b32 s35, s21, s56
	s_cselect_b32 s34, s54, s55
	v_lshl_add_u64 v[146:147], s[30:31], 0, v[138:139]
	s_add_i32 m0, s29, 0xc000
	ds_read_b128 v[188:191], v152
	ds_read_b128 v[192:195], v152 offset:1024
	ds_read_b128 v[196:199], v152 offset:2048
	ds_read_b128 v[200:203], v152 offset:3072
	ds_read_b128 v[204:207], v152 offset:4096
	ds_read_b128 v[208:211], v152 offset:5120
	ds_read_b128 v[212:215], v152 offset:6144
	ds_read_b128 v[216:219], v152 offset:7168
	global_load_lds_dwordx4 v[146:147], off
	v_lshl_add_u64 v[146:147], s[30:31], 0, v[140:141]
	s_add_i32 m0, s29, 0xe000
	s_nop 0
	global_load_lds_dwordx4 v[146:147], off
	s_setprio 0
	s_waitcnt vmcnt(8)
	s_waitcnt lgkmcnt(0)
	s_barrier
	s_setprio 1
	s_waitcnt lgkmcnt(0)
	v_mfma_f32_16x16x32_bf16 v[126:129], v[154:157], v[188:191], v[126:129]
	v_mfma_f32_16x16x32_bf16 v[122:125], v[162:165], v[188:191], v[122:125]
	v_mfma_f32_16x16x32_bf16 v[118:121], v[154:157], v[196:199], v[118:121]
	v_mfma_f32_16x16x32_bf16 v[110:113], v[162:165], v[196:199], v[110:113]
	v_mfma_f32_16x16x32_bf16 v[102:105], v[154:157], v[204:207], v[102:105]
	v_mfma_f32_16x16x32_bf16 v[94:97], v[162:165], v[204:207], v[94:97]
	v_mfma_f32_16x16x32_bf16 v[86:89], v[154:157], v[212:215], v[86:89]
	v_mfma_f32_16x16x32_bf16 v[78:81], v[162:165], v[212:215], v[78:81]
	v_mfma_f32_16x16x32_bf16 v[126:129], v[158:161], v[192:195], v[126:129]
	v_mfma_f32_16x16x32_bf16 v[122:125], v[166:169], v[192:195], v[122:125]
	v_mfma_f32_16x16x32_bf16 v[118:121], v[158:161], v[200:203], v[118:121]
	v_mfma_f32_16x16x32_bf16 v[110:113], v[166:169], v[200:203], v[110:113]
	v_mfma_f32_16x16x32_bf16 v[102:105], v[158:161], v[208:211], v[102:105]
	v_mfma_f32_16x16x32_bf16 v[94:97], v[166:169], v[208:211], v[94:97]
	v_mfma_f32_16x16x32_bf16 v[86:89], v[158:161], v[216:219], v[86:89]
	v_mfma_f32_16x16x32_bf16 v[78:81], v[166:169], v[216:219], v[78:81]
	s_setprio 0
	s_setprio 1
	v_mfma_f32_16x16x32_bf16 v[114:117], v[170:173], v[188:191], v[114:117]
	v_mfma_f32_16x16x32_bf16 v[106:109], v[178:181], v[188:191], v[106:109]
	v_mfma_f32_16x16x32_bf16 v[98:101], v[170:173], v[196:199], v[98:101]
	v_mfma_f32_16x16x32_bf16 v[90:93], v[178:181], v[196:199], v[90:93]
	v_mfma_f32_16x16x32_bf16 v[82:85], v[170:173], v[204:207], v[82:85]
	v_mfma_f32_16x16x32_bf16 v[74:77], v[178:181], v[204:207], v[74:77]
	v_mfma_f32_16x16x32_bf16 v[70:73], v[170:173], v[212:215], v[70:73]
	v_mfma_f32_16x16x32_bf16 v[66:69], v[178:181], v[212:215], v[66:69]
	v_mfma_f32_16x16x32_bf16 v[114:117], v[174:177], v[192:195], v[114:117]
	v_mfma_f32_16x16x32_bf16 v[106:109], v[182:185], v[192:195], v[106:109]
	v_mfma_f32_16x16x32_bf16 v[98:101], v[174:177], v[200:203], v[98:101]
	v_mfma_f32_16x16x32_bf16 v[90:93], v[182:185], v[200:203], v[90:93]
	v_mfma_f32_16x16x32_bf16 v[82:85], v[174:177], v[208:211], v[82:85]
	v_mfma_f32_16x16x32_bf16 v[74:77], v[182:185], v[208:211], v[74:77]
	v_mfma_f32_16x16x32_bf16 v[70:73], v[174:177], v[216:219], v[70:73]
	v_mfma_f32_16x16x32_bf16 v[66:69], v[182:185], v[216:219], v[66:69]
	s_setprio 0
	s_barrier
	s_setprio 2
	s_add_i32 s58, s46, s39
	v_lshl_add_u64 v[146:147], s[34:35], 0, v[132:133]
	s_mov_b32 m0, s58
	ds_read_b128 v[188:191], v152 offset:16384
	ds_read_b128 v[192:195], v152 offset:17408
	ds_read_b128 v[196:199], v152 offset:18432
	ds_read_b128 v[200:203], v152 offset:19456
	ds_read_b128 v[204:207], v152 offset:20480
	ds_read_b128 v[208:211], v152 offset:21504
	ds_read_b128 v[212:215], v152 offset:22528
	ds_read_b128 v[216:219], v152 offset:23552
	global_load_lds_dwordx4 v[146:147], off
	s_add_i32 m0, s58, 0x2000
	s_add_u32 s58, s34, 0x80000
	v_lshl_add_u64 v[220:221], s[34:35], 0, v[136:137]
	s_addc_u32 s59, s35, 0
	s_add_i32 s60, s47, s39
	global_load_lds_dwordx4 v[220:221], off
	v_lshl_add_u64 v[222:223], s[58:59], 0, v[132:133]
	s_mov_b32 m0, s60
	v_lshl_add_u64 v[224:225], s[36:37], 0, v[134:135]
	global_load_lds_dwordx4 v[222:223], off
	v_lshl_add_u64 v[222:223], s[58:59], 0, v[136:137]
	s_add_i32 m0, s60, 0x2000
	s_nop 0
	global_load_lds_dwordx4 v[222:223], off
	v_lshl_add_u64 v[222:223], s[36:37], 0, v[130:131]
	s_mov_b32 m0, s29
	s_nop 0
	global_load_lds_dwordx4 v[222:223], off
	s_mov_b32 m0, s40
	s_nop 0
	global_load_lds_dwordx4 v[224:225], off
	s_setprio 0
	s_waitcnt vmcnt(8)
	s_waitcnt lgkmcnt(0)
	s_barrier
; #define PG8_STAGE(bufoff, gbase, voff) do { _Pragma("unroll") for (int _i = 0; _i < 2; ++_i) \
;         __builtin_amdgcn_global_load_lds((const unsigned*)((const char*)(gbase) + (voff)[_i]), (PG8_LAS unsigned*)(lds + (bufoff) + ldsw + _i * 8192), 16, 0, 0); } while (0)
; #define PG8_LDA(dst, b, h) do { _Pragma("unroll") for (int m = 0; m < 4; ++m) _Pragma("unroll") for (int k = 0; k < 2; ++k) dst[m][k] = *(const PG8_LAS bf16x8*)(lds + PG8_SA(b, h) + aoff + m * 2048 + k * 1024); } while (0)
; #define PG8_LDB(dst, b, h) do { _Pragma("unroll") for (int n = 0; n < 2; ++n) _Pragma("unroll") for (int k = 0; k < 2; ++k) dst[n][k] = *(const PG8_LAS bf16x8*)(lds + PG8_SB(b, h) + boff + n * 2048 + k * 1024); } while (0)
; #define PG8_MMA(ai, bj, At, Bt) do { __builtin_amdgcn_s_setprio(1); _Pragma("unroll") for (int m = 0; m < 4; ++m) _Pragma("unroll") for (int n = 0; n < 2; ++n) _Pragma("unroll") for (int k = 0; k < 2; ++k) \
;         acc[ai][bj][m][n] = __builtin_amdgcn_mfma_f32_16x16x32_bf16(Bt[n][k], At[m][k], acc[ai][bj][m][n], 0, 0, 0); __builtin_amdgcn_s_setprio(0); } while (0)
; #define PG8_WAIT_V(n) asm volatile("s_waitcnt vmcnt(" #n ")" ::: "memory")
; #define PG8_WAIT_L(n) asm volatile("s_waitcnt lgkmcnt(" #n ")" ::: "memory")
; #define PG8_BAR __builtin_amdgcn_s_barrier()
; #define PG8_SCHED __builtin_amdgcn_sched_barrier(0)
; #define PG8_STAGE(bufoff, gbase, voff) do { _Pragma("unroll") for (int _i = 0; _i < 2; ++_i) \
;         __builtin_amdgcn_global_load_lds((const unsigned*)((const char*)(gbase) + (voff)[_i]), (PG8_LAS unsigned*)(lds + (bufoff) + ldsw + _i * 8192), 16, 0, 0); } while (0)
; #define PG8_WAIT_V(n) asm volatile("s_waitcnt vmcnt(" #n ")" ::: "memory")
; #define PG8_WAIT_L(n) asm volatile("s_waitcnt lgkmcnt(" #n ")" ::: "memory")
; #define PG8_BAR __builtin_amdgcn_s_barrier()
; template <class Epi, class Sched, bool ALIGN_EPI = false, bool SP2 = false>
; __device__ __forceinline__ void gemm_phase(PG8_LAS unsigned char* lds, const Gemm g, const Sched& S, const Epi& E) {
;     ...
;             PG8_WAIT_V(8); PG8_WAIT_L(0); PG8_BAR; PG8_MMA(1, 0, At, B0); PG8_MMA(1, 1, At, B1); PG8_BAR; PG8_SCHED;
;             PG8_LDB(B0, 1, 0); PG8_LDB(B1, 1, 1); PG8_SCHED; PG8_LDA(At, 1, 0); PG8_STAGE(PG8_SA(0, 1), a2 + hstep, voffA);
;             PG8_WAIT_V(8); PG8_WAIT_L(0); PG8_BAR; PG8_MMA(0, 0, At, B0); PG8_MMA(0, 1, At, B1); PG8_BAR; PG8_SCHED;
	s_setprio 1
	s_waitcnt lgkmcnt(0)
	v_mfma_f32_16x16x32_bf16 v[62:65], v[154:157], v[188:191], v[62:65]
	v_mfma_f32_16x16x32_bf16 v[58:61], v[162:165], v[188:191], v[58:61]
	v_mfma_f32_16x16x32_bf16 v[54:57], v[154:157], v[196:199], v[54:57]
	v_mfma_f32_16x16x32_bf16 v[46:49], v[162:165], v[196:199], v[46:49]
	v_mfma_f32_16x16x32_bf16 v[38:41], v[154:157], v[204:207], v[38:41]
	v_mfma_f32_16x16x32_bf16 v[30:33], v[162:165], v[204:207], v[30:33]
	v_mfma_f32_16x16x32_bf16 v[22:25], v[154:157], v[212:215], v[22:25]
	v_mfma_f32_16x16x32_bf16 v[14:17], v[162:165], v[212:215], v[14:17]
	v_mfma_f32_16x16x32_bf16 v[62:65], v[158:161], v[192:195], v[62:65]
	v_mfma_f32_16x16x32_bf16 v[58:61], v[166:169], v[192:195], v[58:61]
	v_mfma_f32_16x16x32_bf16 v[54:57], v[158:161], v[200:203], v[54:57]
	v_mfma_f32_16x16x32_bf16 v[46:49], v[166:169], v[200:203], v[46:49]
	v_mfma_f32_16x16x32_bf16 v[38:41], v[158:161], v[208:211], v[38:41]
	v_mfma_f32_16x16x32_bf16 v[30:33], v[166:169], v[208:211], v[30:33]
	v_mfma_f32_16x16x32_bf16 v[22:25], v[158:161], v[216:219], v[22:25]
	v_mfma_f32_16x16x32_bf16 v[14:17], v[166:169], v[216:219], v[14:17]
	s_setprio 0
	s_setprio 1
	v_mfma_f32_16x16x32_bf16 v[50:53], v[170:173], v[188:191], v[50:53]
	v_mfma_f32_16x16x32_bf16 v[42:45], v[178:181], v[188:191], v[42:45]
	v_mfma_f32_16x16x32_bf16 v[34:37], v[170:173], v[196:199], v[34:37]
	v_mfma_f32_16x16x32_bf16 v[26:29], v[178:181], v[196:199], v[26:29]
	v_mfma_f32_16x16x32_bf16 v[18:21], v[170:173], v[204:207], v[18:21]
	v_mfma_f32_16x16x32_bf16 v[10:13], v[178:181], v[204:207], v[10:13]
	v_mfma_f32_16x16x32_bf16 v[6:9], v[170:173], v[212:215], v[6:9]
	v_mfma_f32_16x16x32_bf16 v[2:5], v[178:181], v[212:215], v[2:5]
	v_mfma_f32_16x16x32_bf16 v[50:53], v[174:177], v[192:195], v[50:53]
	v_mfma_f32_16x16x32_bf16 v[42:45], v[182:185], v[192:195], v[42:45]
	v_mfma_f32_16x16x32_bf16 v[34:37], v[174:177], v[200:203], v[34:37]
	v_mfma_f32_16x16x32_bf16 v[26:29], v[182:185], v[200:203], v[26:29]
	v_mfma_f32_16x16x32_bf16 v[18:21], v[174:177], v[208:211], v[18:21]
	v_mfma_f32_16x16x32_bf16 v[10:13], v[182:185], v[208:211], v[10:13]
	v_mfma_f32_16x16x32_bf16 v[6:9], v[174:177], v[216:219], v[6:9]
	v_mfma_f32_16x16x32_bf16 v[2:5], v[182:185], v[216:219], v[2:5]
	s_setprio 0
	s_barrier
	s_setprio 2
	s_add_i32 s58, 0, 0x18000
	v_add_u32_e32 v153, s58, v148
	s_add_i32 s59, 0, 0x1c000
	ds_read_b128 v[154:157], v153
	ds_read_b128 v[158:161], v153 offset:1024
	ds_read_b128 v[162:165], v153 offset:2048
	ds_read_b128 v[166:169], v153 offset:3072
	v_add_u32_e32 v153, s59, v148
	ds_read_b128 v[170:173], v153
	ds_read_b128 v[174:177], v153 offset:1024
	ds_read_b128 v[178:181], v153 offset:2048
	ds_read_b128 v[182:185], v153 offset:3072
	s_add_u32 s36, s36, 0x80000
	s_addc_u32 s37, s37, 0
	s_mov_b32 m0, s41
	v_lshl_add_u64 v[226:227], s[36:37], 0, v[130:131]
	ds_read_b128 v[188:191], v152 offset:32768
	ds_read_b128 v[192:195], v152 offset:33792
	ds_read_b128 v[196:199], v152 offset:34816
	ds_read_b128 v[200:203], v152 offset:35840
	ds_read_b128 v[204:207], v152 offset:36864
	ds_read_b128 v[208:211], v152 offset:37888
	ds_read_b128 v[212:215], v152 offset:38912
	ds_read_b128 v[216:219], v152 offset:39936
	global_load_lds_dwordx4 v[226:227], off
	v_lshl_add_u64 v[226:227], s[36:37], 0, v[134:135]
	s_mov_b32 m0, s42
	s_nop 0
	global_load_lds_dwordx4 v[226:227], off
	s_setprio 0
	s_waitcnt vmcnt(8)
	s_waitcnt lgkmcnt(0)
	s_barrier
	s_setprio 1
	s_waitcnt lgkmcnt(0)
	v_mfma_f32_16x16x32_bf16 v[126:129], v[154:157], v[188:191], v[126:129]
	v_mfma_f32_16x16x32_bf16 v[122:125], v[162:165], v[188:191], v[122:125]
	v_mfma_f32_16x16x32_bf16 v[118:121], v[154:157], v[196:199], v[118:121]
	v_mfma_f32_16x16x32_bf16 v[110:113], v[162:165], v[196:199], v[110:113]
	v_mfma_f32_16x16x32_bf16 v[102:105], v[154:157], v[204:207], v[102:105]
	v_mfma_f32_16x16x32_bf16 v[94:97], v[162:165], v[204:207], v[94:97]
	v_mfma_f32_16x16x32_bf16 v[86:89], v[154:157], v[212:215], v[86:89]
	v_mfma_f32_16x16x32_bf16 v[78:81], v[162:165], v[212:215], v[78:81]
	v_mfma_f32_16x16x32_bf16 v[126:129], v[158:161], v[192:195], v[126:129]
	v_mfma_f32_16x16x32_bf16 v[122:125], v[166:169], v[192:195], v[122:125]
	v_mfma_f32_16x16x32_bf16 v[118:121], v[158:161], v[200:203], v[118:121]
	v_mfma_f32_16x16x32_bf16 v[110:113], v[166:169], v[200:203], v[110:113]
	v_mfma_f32_16x16x32_bf16 v[102:105], v[158:161], v[208:211], v[102:105]
	v_mfma_f32_16x16x32_bf16 v[94:97], v[166:169], v[208:211], v[94:97]
	v_mfma_f32_16x16x32_bf16 v[86:89], v[158:161], v[216:219], v[86:89]
	v_mfma_f32_16x16x32_bf16 v[78:81], v[166:169], v[216:219], v[78:81]
	s_setprio 0
	s_setprio 1
	v_mfma_f32_16x16x32_bf16 v[114:117], v[170:173], v[188:191], v[114:117]
	v_mfma_f32_16x16x32_bf16 v[106:109], v[178:181], v[188:191], v[106:109]
	v_mfma_f32_16x16x32_bf16 v[98:101], v[170:173], v[196:199], v[98:101]
	v_mfma_f32_16x16x32_bf16 v[90:93], v[178:181], v[196:199], v[90:93]
	v_mfma_f32_16x16x32_bf16 v[82:85], v[170:173], v[204:207], v[82:85]
	v_mfma_f32_16x16x32_bf16 v[74:77], v[178:181], v[204:207], v[74:77]
	v_mfma_f32_16x16x32_bf16 v[70:73], v[170:173], v[212:215], v[70:73]
	v_mfma_f32_16x16x32_bf16 v[66:69], v[178:181], v[212:215], v[66:69]
	v_mfma_f32_16x16x32_bf16 v[114:117], v[174:177], v[192:195], v[114:117]
	v_mfma_f32_16x16x32_bf16 v[106:109], v[182:185], v[192:195], v[106:109]
	v_mfma_f32_16x16x32_bf16 v[98:101], v[174:177], v[200:203], v[98:101]
	v_mfma_f32_16x16x32_bf16 v[90:93], v[182:185], v[200:203], v[90:93]
	v_mfma_f32_16x16x32_bf16 v[82:85], v[174:177], v[208:211], v[82:85]
	v_mfma_f32_16x16x32_bf16 v[74:77], v[182:185], v[208:211], v[74:77]
	v_mfma_f32_16x16x32_bf16 v[70:73], v[174:177], v[216:219], v[70:73]
	v_mfma_f32_16x16x32_bf16 v[66:69], v[182:185], v[216:219], v[66:69]
	s_setprio 0
	s_barrier
; #define PG8_STAGE(bufoff, gbase, voff) do { _Pragma("unroll") for (int _i = 0; _i < 2; ++_i) \
;         __builtin_amdgcn_global_load_lds((const unsigned*)((const char*)(gbase) + (voff)[_i]), (PG8_LAS unsigned*)(lds + (bufoff) + ldsw + _i * 8192), 16, 0, 0); } while (0)
; #define PG8_LDA(dst, b, h) do { _Pragma("unroll") for (int m = 0; m < 4; ++m) _Pragma("unroll") for (int k = 0; k < 2; ++k) dst[m][k] = *(const PG8_LAS bf16x8*)(lds + PG8_SA(b, h) + aoff + m * 2048 + k * 1024); } while (0)
; #define PG8_MMA(ai, bj, At, Bt) do { __builtin_amdgcn_s_setprio(1); _Pragma("unroll") for (int m = 0; m < 4; ++m) _Pragma("unroll") for (int n = 0; n < 2; ++n) _Pragma("unroll") for (int k = 0; k < 2; ++k) \
;         acc[ai][bj][m][n] = __builtin_amdgcn_mfma_f32_16x16x32_bf16(Bt[n][k], At[m][k], acc[ai][bj][m][n], 0, 0, 0); __builtin_amdgcn_s_setprio(0); } while (0)
; #define PG8_WAIT_V(n) asm volatile("s_waitcnt vmcnt(" #n ")" ::: "memory")
; #define PG8_WAIT_L(n) asm volatile("s_waitcnt lgkmcnt(" #n ")" ::: "memory")
; #define PG8_BAR __builtin_amdgcn_s_barrier()
; #define PG8_SCHED __builtin_amdgcn_sched_barrier(0)
; #define PG8_STAGE(bufoff, gbase, voff) do { _Pragma("unroll") for (int _i = 0; _i < 2; ++_i) \
;         __builtin_amdgcn_global_load_lds((const unsigned*)((const char*)(gbase) + (voff)[_i]), (PG8_LAS unsigned*)(lds + (bufoff) + ldsw + _i * 8192), 16, 0, 0); } while (0)
; #define PG8_LDA(dst, b, h) do { _Pragma("unroll") for (int m = 0; m < 4; ++m) _Pragma("unroll") for (int k = 0; k < 2; ++k) dst[m][k] = *(const PG8_LAS bf16x8*)(lds + PG8_SA(b, h) + aoff + m * 2048 + k * 1024); } while (0)
; #define PG8_WAIT_V(n) asm volatile("s_waitcnt vmcnt(" #n ")" ::: "memory")
; #define PG8_WAIT_L(n) asm volatile("s_waitcnt lgkmcnt(" #n ")" ::: "memory")
; #define PG8_BAR __builtin_amdgcn_s_barrier()
; template <class Epi, class Sched, bool ALIGN_EPI = false, bool SP2 = false>
; __device__ __forceinline__ void gemm_phase(PG8_LAS unsigned char* lds, const Gemm g, const Sched& S, const Epi& E) {
;     ...
;             PG8_LDA(At, 1, 1); PG8_STAGE(PG8_SB(1, 0), b3, voffB); PG8_STAGE(PG8_SB(1, 1), b3 + hstep, voffB); PG8_STAGE(PG8_SA(1, 0), a3, voffA);
;             PG8_WAIT_V(8); PG8_WAIT_L(0); PG8_BAR; PG8_MMA(1, 0, At, B0); PG8_MMA(1, 1, At, B1); PG8_BAR; PG8_SCHED;
;     ...
;         if constexpr (ALIGN_EPI) { if (wr == 0) PG8_BAR; }
	s_setprio 2
	s_add_i32 s36, s58, s39
	v_lshl_add_u64 v[146:147], v[146:147], 0, s[10:11]
	s_mov_b32 m0, s36
	ds_read_b128 v[188:191], v152 offset:49152
	ds_read_b128 v[192:195], v152 offset:50176
	ds_read_b128 v[196:199], v152 offset:51200
	ds_read_b128 v[200:203], v152 offset:52224
	ds_read_b128 v[204:207], v152 offset:53248
	ds_read_b128 v[208:211], v152 offset:54272
	ds_read_b128 v[212:215], v152 offset:55296
	ds_read_b128 v[216:219], v152 offset:56320
	global_load_lds_dwordx4 v[146:147], off
	s_add_i32 m0, s36, 0x2000
	s_add_u32 s34, s34, 0x80080
	v_lshl_add_u64 v[146:147], v[220:221], 0, s[10:11]
	s_addc_u32 s35, s35, 0
	s_add_i32 s36, s59, s39
	global_load_lds_dwordx4 v[146:147], off
	v_lshl_add_u64 v[146:147], s[34:35], 0, v[132:133]
	s_mov_b32 m0, s36
	s_nop 0
	global_load_lds_dwordx4 v[146:147], off
	v_lshl_add_u64 v[146:147], s[34:35], 0, v[136:137]
	s_add_i32 m0, s36, 0x2000
	s_nop 0
	global_load_lds_dwordx4 v[146:147], off
	v_lshl_add_u64 v[146:147], v[222:223], 0, s[10:11]
	s_mov_b32 m0, s44
	s_nop 0
	global_load_lds_dwordx4 v[146:147], off
	v_lshl_add_u64 v[146:147], v[224:225], 0, s[10:11]
	s_mov_b32 m0, s45
	s_nop 0
	global_load_lds_dwordx4 v[146:147], off
	s_setprio 0
	s_waitcnt vmcnt(8)
	s_waitcnt lgkmcnt(0)
	s_barrier
	s_setprio 1
	s_waitcnt lgkmcnt(0)
	v_mfma_f32_16x16x32_bf16 v[62:65], v[154:157], v[188:191], v[62:65]
	v_mfma_f32_16x16x32_bf16 v[58:61], v[162:165], v[188:191], v[58:61]
	v_mfma_f32_16x16x32_bf16 v[54:57], v[154:157], v[196:199], v[54:57]
	v_mfma_f32_16x16x32_bf16 v[46:49], v[162:165], v[196:199], v[46:49]
	v_mfma_f32_16x16x32_bf16 v[38:41], v[154:157], v[204:207], v[38:41]
	v_mfma_f32_16x16x32_bf16 v[30:33], v[162:165], v[204:207], v[30:33]
	v_mfma_f32_16x16x32_bf16 v[22:25], v[154:157], v[212:215], v[22:25]
	v_mfma_f32_16x16x32_bf16 v[14:17], v[162:165], v[212:215], v[14:17]
	v_mfma_f32_16x16x32_bf16 v[62:65], v[158:161], v[192:195], v[62:65]
	v_mfma_f32_16x16x32_bf16 v[58:61], v[166:169], v[192:195], v[58:61]
	v_mfma_f32_16x16x32_bf16 v[54:57], v[158:161], v[200:203], v[54:57]
	v_mfma_f32_16x16x32_bf16 v[46:49], v[166:169], v[200:203], v[46:49]
	v_mfma_f32_16x16x32_bf16 v[38:41], v[158:161], v[208:211], v[38:41]
	v_mfma_f32_16x16x32_bf16 v[30:33], v[166:169], v[208:211], v[30:33]
	v_mfma_f32_16x16x32_bf16 v[22:25], v[158:161], v[216:219], v[22:25]
	v_mfma_f32_16x16x32_bf16 v[14:17], v[166:169], v[216:219], v[14:17]
	s_setprio 0
	s_setprio 1
	v_mfma_f32_16x16x32_bf16 v[50:53], v[170:173], v[188:191], v[50:53]
	v_mfma_f32_16x16x32_bf16 v[42:45], v[178:181], v[188:191], v[42:45]
	v_mfma_f32_16x16x32_bf16 v[34:37], v[170:173], v[196:199], v[34:37]
	v_mfma_f32_16x16x32_bf16 v[26:29], v[178:181], v[196:199], v[26:29]
	v_mfma_f32_16x16x32_bf16 v[18:21], v[170:173], v[204:207], v[18:21]
	v_mfma_f32_16x16x32_bf16 v[10:13], v[178:181], v[204:207], v[10:13]
	v_mfma_f32_16x16x32_bf16 v[6:9], v[170:173], v[212:215], v[6:9]
	v_mfma_f32_16x16x32_bf16 v[2:5], v[178:181], v[212:215], v[2:5]
	v_mfma_f32_16x16x32_bf16 v[50:53], v[174:177], v[192:195], v[50:53]
	v_mfma_f32_16x16x32_bf16 v[42:45], v[182:185], v[192:195], v[42:45]
	v_mfma_f32_16x16x32_bf16 v[34:37], v[174:177], v[200:203], v[34:37]
	v_mfma_f32_16x16x32_bf16 v[26:29], v[182:185], v[200:203], v[26:29]
	v_mfma_f32_16x16x32_bf16 v[18:21], v[174:177], v[208:211], v[18:21]
	v_mfma_f32_16x16x32_bf16 v[10:13], v[182:185], v[208:211], v[10:13]
	v_mfma_f32_16x16x32_bf16 v[6:9], v[174:177], v[216:219], v[6:9]
	v_mfma_f32_16x16x32_bf16 v[2:5], v[182:185], v[216:219], v[2:5]
	s_setprio 0
	s_barrier
	s_setprio 2
	s_add_i32 s57, s57, 2
	s_add_u32 s30, s30, 0x100
	s_addc_u32 s31, s31, 0
	s_add_u32 s55, s55, 0x100
	s_addc_u32 s56, s56, 0
	s_cmp_gt_u32 s57, 29
	s_cbranch_scc0 .LBB0_1011
	s_and_b64 vcc, exec, s[12:13]
	s_cbranch_vccz .LBB0_1014
	s_barrier

; #define PG8_STAGE(bufoff, gbase, voff) do { _Pragma("unroll") for (int _i = 0; _i < 2; ++_i) \
;         __builtin_amdgcn_global_load_lds((const unsigned*)((const char*)(gbase) + (voff)[_i]), (PG8_LAS unsigned*)(lds + (bufoff) + ldsw + _i * 8192), 16, 0, 0); } while (0)
; #define PG8_LDA(dst, b, h) do { _Pragma("unroll") for (int m = 0; m < 4; ++m) _Pragma("unroll") for (int k = 0; k < 2; ++k) dst[m][k] = *(const PG8_LAS bf16x8*)(lds + PG8_SA(b, h) + aoff + m * 2048 + k * 1024); } while (0)
; #define PG8_LDB(dst, b, h) do { _Pragma("unroll") for (int n = 0; n < 2; ++n) _Pragma("unroll") for (int k = 0; k < 2; ++k) dst[n][k] = *(const PG8_LAS bf16x8*)(lds + PG8_SB(b, h) + boff + n * 2048 + k * 1024); } while (0)
; #define PG8_MMA(ai, bj, At, Bt) do { __builtin_amdgcn_s_setprio(1); _Pragma("unroll") for (int m = 0; m < 4; ++m) _Pragma("unroll") for (int n = 0; n < 2; ++n) _Pragma("unroll") for (int k = 0; k < 2; ++k) \
;         acc[ai][bj][m][n] = __builtin_amdgcn_mfma_f32_16x16x32_bf16(Bt[n][k], At[m][k], acc[ai][bj][m][n], 0, 0, 0); __builtin_amdgcn_s_setprio(0); } while (0)
; #define PG8_WAIT_V(n) asm volatile("s_waitcnt vmcnt(" #n ")" ::: "memory")
; #define PG8_BAR __builtin_amdgcn_s_barrier()
; template <class Epi, class Sched>
; __device__ __forceinline__ void gemm_phase_gather(PG8_LAS unsigned char* lds, const Gemm g, const int* __restrict__ gidx, PG8_LAS int* itab  , const Sched& S, const Epi& E) {
;     ...
;             const bool last = (t == nt - 2);
;             const char* a1 = gA + (size_t)(t + 1) * kstep;
;             const char* a2 = last ? gA : gA + (size_t)(t + 2) * kstep; const char* b2 = last ? nB : cB + (size_t)(t + 2) * kstep;
;             const char* a3 = a2 + kstep; const char* b3 = b2 + kstep;
;             unsigned vo2[2][2];
; #pragma unroll
;             for (int _h = 0; _h < 2; ++_h)
; #pragma unroll
;                 for (int _i = 0; _i < 2; ++_i) vo2[_h][_i] = last ? nvo[_h][_i] : cvo[_h][_i];
;             if (last && has_next) S.a_ready(nxt);
;             PG8_LDB(B0, 0, 0); PG8_LDB(B1, 0, 1); PG8_SCHED; PG8_LDA(At, 0, 0); PG8_STAGE(PG8_SA(1, 1), a1, cvo[1]);
;             PG8_WAIT_V(8); PG8_WAIT_L(0); PG8_BAR; PG8_MMA(0, 0, At, B0); PG8_MMA(0, 1, At, B1); PG8_BAR; PG8_SCHED;
;             PG8_LDA(At, 0, 1); PG8_STAGE(PG8_SB(0, 0), b2, voffB); PG8_STAGE(PG8_SB(0, 1), b2 + hstep, voffB); PG8_STAGE(PG8_SA(0, 0), a2, vo2[0]);
.LBB0_1278:
	s_setprio 2
	ds_read_b128 v[158:161], v150
	ds_read_b128 v[162:165], v150 offset:1024
	ds_read_b128 v[166:169], v150 offset:2048
	ds_read_b128 v[170:173], v150 offset:3072
	ds_read_b128 v[174:177], v151
	ds_read_b128 v[178:181], v151 offset:1024
	ds_read_b128 v[182:185], v151 offset:2048
	ds_read_b128 v[188:191], v151 offset:3072
	s_add_u32 s24, s0, s22
	s_addc_u32 s25, s1, s23
	s_add_u32 s26, s24, 0xe800100
	s_addc_u32 s27, s25, 0
	s_add_u32 s50, s47, s22
	s_addc_u32 s51, s48, s23
	s_cmpk_eq_i32 s22, 0xf00
	s_cselect_b64 vcc, -1, 0
	s_and_b64 s[24:25], vcc, exec
	v_cndmask_b32_e32 v134, v157, v153, vcc
	s_cselect_b32 s27, s3, s27
	s_cselect_b32 s26, s2, s26
	v_cndmask_b32_e32 v224, v140, v154, vcc
	v_cndmask_b32_e32 v137, v138, v155, vcc
	v_cndmask_b32_e32 v139, v136, v156, vcc
	s_cselect_b32 s25, s17, s51
	s_cselect_b32 s24, s46, s50
	s_mov_b32 m0, s43
	v_lshl_add_u64 v[226:227], v[144:145], 0, s[22:23]
	ds_read_b128 v[192:195], v152
	ds_read_b128 v[196:199], v152 offset:1024
	ds_read_b128 v[200:203], v152 offset:2048
	ds_read_b128 v[204:207], v152 offset:3072
	ds_read_b128 v[208:211], v152 offset:4096
	ds_read_b128 v[212:215], v152 offset:5120
	ds_read_b128 v[216:219], v152 offset:6144
	ds_read_b128 v[220:223], v152 offset:7168
	global_load_lds_dwordx4 v[226:227], off
	v_lshl_add_u64 v[226:227], v[142:143], 0, s[22:23]
	s_add_i32 m0, s21, 0xe000
	s_nop 0
	global_load_lds_dwordx4 v[226:227], off
	s_setprio 0
	s_waitcnt vmcnt(8)
	s_waitcnt lgkmcnt(0)
	s_barrier
	s_setprio 1
	s_waitcnt lgkmcnt(0)
	v_mfma_f32_16x16x32_bf16 v[126:129], v[158:161], v[192:195], v[126:129]
	v_mfma_f32_16x16x32_bf16 v[122:125], v[166:169], v[192:195], v[122:125]
	v_mfma_f32_16x16x32_bf16 v[110:113], v[158:161], v[200:203], v[110:113]
	v_mfma_f32_16x16x32_bf16 v[106:109], v[166:169], v[200:203], v[106:109]
	v_mfma_f32_16x16x32_bf16 v[94:97], v[158:161], v[208:211], v[94:97]
	v_mfma_f32_16x16x32_bf16 v[90:93], v[166:169], v[208:211], v[90:93]
	v_mfma_f32_16x16x32_bf16 v[78:81], v[158:161], v[216:219], v[78:81]
	v_mfma_f32_16x16x32_bf16 v[74:77], v[166:169], v[216:219], v[74:77]
	v_mfma_f32_16x16x32_bf16 v[126:129], v[162:165], v[196:199], v[126:129]
	v_mfma_f32_16x16x32_bf16 v[122:125], v[170:173], v[196:199], v[122:125]
	v_mfma_f32_16x16x32_bf16 v[110:113], v[162:165], v[204:207], v[110:113]
	v_mfma_f32_16x16x32_bf16 v[106:109], v[170:173], v[204:207], v[106:109]
	v_mfma_f32_16x16x32_bf16 v[94:97], v[162:165], v[212:215], v[94:97]
	v_mfma_f32_16x16x32_bf16 v[90:93], v[170:173], v[212:215], v[90:93]
	v_mfma_f32_16x16x32_bf16 v[78:81], v[162:165], v[220:223], v[78:81]
	v_mfma_f32_16x16x32_bf16 v[74:77], v[170:173], v[220:223], v[74:77]
	s_setprio 0
	s_setprio 1
	v_mfma_f32_16x16x32_bf16 v[118:121], v[174:177], v[192:195], v[118:121]
	v_mfma_f32_16x16x32_bf16 v[114:117], v[182:185], v[192:195], v[114:117]
	v_mfma_f32_16x16x32_bf16 v[102:105], v[174:177], v[200:203], v[102:105]
	v_mfma_f32_16x16x32_bf16 v[98:101], v[182:185], v[200:203], v[98:101]
	v_mfma_f32_16x16x32_bf16 v[86:89], v[174:177], v[208:211], v[86:89]
	v_mfma_f32_16x16x32_bf16 v[82:85], v[182:185], v[208:211], v[82:85]
	v_mfma_f32_16x16x32_bf16 v[70:73], v[174:177], v[216:219], v[70:73]
	v_mfma_f32_16x16x32_bf16 v[66:69], v[182:185], v[216:219], v[66:69]
	v_mfma_f32_16x16x32_bf16 v[118:121], v[178:181], v[196:199], v[118:121]
	v_mfma_f32_16x16x32_bf16 v[114:117], v[188:191], v[196:199], v[114:117]
	v_mfma_f32_16x16x32_bf16 v[102:105], v[178:181], v[204:207], v[102:105]
	v_mfma_f32_16x16x32_bf16 v[98:101], v[188:191], v[204:207], v[98:101]
	v_mfma_f32_16x16x32_bf16 v[86:89], v[178:181], v[212:215], v[86:89]
	v_mfma_f32_16x16x32_bf16 v[82:85], v[188:191], v[212:215], v[82:85]
	v_mfma_f32_16x16x32_bf16 v[70:73], v[178:181], v[220:223], v[70:73]
	v_mfma_f32_16x16x32_bf16 v[66:69], v[188:191], v[220:223], v[66:69]
	s_setprio 0
	s_barrier
	s_setprio 2
	s_add_i32 s50, s38, s28
	v_lshl_add_u64 v[226:227], s[24:25], 0, v[130:131]
	s_mov_b32 m0, s50
	ds_read_b128 v[192:195], v152 offset:16384
	ds_read_b128 v[196:199], v152 offset:17408
	ds_read_b128 v[200:203], v152 offset:18432
	ds_read_b128 v[204:207], v152 offset:19456
	ds_read_b128 v[208:211], v152 offset:20480
	ds_read_b128 v[212:215], v152 offset:21504
	ds_read_b128 v[216:219], v152 offset:22528
	ds_read_b128 v[220:223], v152 offset:23552
	global_load_lds_dwordx4 v[226:227], off
	s_add_i32 m0, s50, 0x2000
	s_add_u32 s50, s24, 0x80000
	v_lshl_add_u64 v[228:229], s[24:25], 0, v[132:133]
	s_addc_u32 s51, s25, 0
	s_add_i32 s52, s39, s28
	global_load_lds_dwordx4 v[228:229], off
	v_lshl_add_u64 v[230:231], s[50:51], 0, v[130:131]
	s_mov_b32 m0, s52
	v_mov_b32_e32 v225, v135
	global_load_lds_dwordx4 v[230:231], off
	v_lshl_add_u64 v[230:231], s[50:51], 0, v[132:133]
	s_add_i32 m0, s52, 0x2000
	s_nop 0
	global_load_lds_dwordx4 v[230:231], off
	s_mov_b32 m0, s21
	v_lshl_add_u64 v[230:231], s[26:27], 0, v[134:135]
	global_load_lds_dwordx4 v134, s[26:27]
	s_mov_b32 m0, s31
	s_nop 0
	global_load_lds_dwordx4 v224, s[26:27]
	s_setprio 0
	s_waitcnt vmcnt(8)
	s_waitcnt lgkmcnt(0)
	v_lshl_add_u64 v[224:225], s[26:27], 0, v[224:225]
	s_barrier
; #define PG8_STAGE(bufoff, gbase, voff) do { _Pragma("unroll") for (int _i = 0; _i < 2; ++_i) \
;         __builtin_amdgcn_global_load_lds((const unsigned*)((const char*)(gbase) + (voff)[_i]), (PG8_LAS unsigned*)(lds + (bufoff) + ldsw + _i * 8192), 16, 0, 0); } while (0)
; #define PG8_LDA(dst, b, h) do { _Pragma("unroll") for (int m = 0; m < 4; ++m) _Pragma("unroll") for (int k = 0; k < 2; ++k) dst[m][k] = *(const PG8_LAS bf16x8*)(lds + PG8_SA(b, h) + aoff + m * 2048 + k * 1024); } while (0)
; #define PG8_LDB(dst, b, h) do { _Pragma("unroll") for (int n = 0; n < 2; ++n) _Pragma("unroll") for (int k = 0; k < 2; ++k) dst[n][k] = *(const PG8_LAS bf16x8*)(lds + PG8_SB(b, h) + boff + n * 2048 + k * 1024); } while (0)
; #define PG8_MMA(ai, bj, At, Bt) do { __builtin_amdgcn_s_setprio(1); _Pragma("unroll") for (int m = 0; m < 4; ++m) _Pragma("unroll") for (int n = 0; n < 2; ++n) _Pragma("unroll") for (int k = 0; k < 2; ++k) \
;         acc[ai][bj][m][n] = __builtin_amdgcn_mfma_f32_16x16x32_bf16(Bt[n][k], At[m][k], acc[ai][bj][m][n], 0, 0, 0); __builtin_amdgcn_s_setprio(0); } while (0)
; #define PG8_WAIT_V(n) asm volatile("s_waitcnt vmcnt(" #n ")" ::: "memory")
; #define PG8_WAIT_L(n) asm volatile("s_waitcnt lgkmcnt(" #n ")" ::: "memory")
; #define PG8_BAR __builtin_amdgcn_s_barrier()
; #define PG8_SCHED __builtin_amdgcn_sched_barrier(0)
; #define PG8_STAGE(bufoff, gbase, voff) do { _Pragma("unroll") for (int _i = 0; _i < 2; ++_i) \
;         __builtin_amdgcn_global_load_lds((const unsigned*)((const char*)(gbase) + (voff)[_i]), (PG8_LAS unsigned*)(lds + (bufoff) + ldsw + _i * 8192), 16, 0, 0); } while (0)
; #define PG8_WAIT_V(n) asm volatile("s_waitcnt vmcnt(" #n ")" ::: "memory")
; #define PG8_WAIT_L(n) asm volatile("s_waitcnt lgkmcnt(" #n ")" ::: "memory")
; #define PG8_BAR __builtin_amdgcn_s_barrier()
; template <class Epi, class Sched>
; __device__ __forceinline__ void gemm_phase_gather(PG8_LAS unsigned char* lds, const Gemm g, const int* __restrict__ gidx, PG8_LAS int* itab  , const Sched& S, const Epi& E) {
;     ...
;             PG8_WAIT_V(8); PG8_WAIT_L(0); PG8_BAR; PG8_MMA(1, 0, At, B0); PG8_MMA(1, 1, At, B1); PG8_BAR; PG8_SCHED;
;             PG8_LDB(B0, 1, 0); PG8_LDB(B1, 1, 1); PG8_SCHED; PG8_LDA(At, 1, 0); PG8_STAGE(PG8_SA(0, 1), a2, vo2[1]);
;             PG8_WAIT_V(8); PG8_WAIT_L(0); PG8_BAR; PG8_MMA(0, 0, At, B0); PG8_MMA(0, 1, At, B1); PG8_BAR; PG8_SCHED;
	s_setprio 1
	s_waitcnt lgkmcnt(0)
	v_mfma_f32_16x16x32_bf16 v[62:65], v[158:161], v[192:195], v[62:65]
	v_mfma_f32_16x16x32_bf16 v[58:61], v[166:169], v[192:195], v[58:61]
	v_mfma_f32_16x16x32_bf16 v[46:49], v[158:161], v[200:203], v[46:49]
	v_mfma_f32_16x16x32_bf16 v[38:41], v[166:169], v[200:203], v[38:41]
	v_mfma_f32_16x16x32_bf16 v[14:17], v[158:161], v[208:211], v[14:17]
	v_mfma_f32_16x16x32_bf16 v[10:13], v[166:169], v[208:211], v[10:13]
	v_mfma_f32_16x16x32_bf16 v[6:9], v[158:161], v[216:219], v[6:9]
	v_mfma_f32_16x16x32_bf16 v[2:5], v[166:169], v[216:219], v[2:5]
	v_mfma_f32_16x16x32_bf16 v[62:65], v[162:165], v[196:199], v[62:65]
	v_mfma_f32_16x16x32_bf16 v[58:61], v[170:173], v[196:199], v[58:61]
	v_mfma_f32_16x16x32_bf16 v[46:49], v[162:165], v[204:207], v[46:49]
	v_mfma_f32_16x16x32_bf16 v[38:41], v[170:173], v[204:207], v[38:41]
	v_mfma_f32_16x16x32_bf16 v[14:17], v[162:165], v[212:215], v[14:17]
	v_mfma_f32_16x16x32_bf16 v[10:13], v[170:173], v[212:215], v[10:13]
	v_mfma_f32_16x16x32_bf16 v[6:9], v[162:165], v[220:223], v[6:9]
	v_mfma_f32_16x16x32_bf16 v[2:5], v[170:173], v[220:223], v[2:5]
	s_setprio 0
	s_setprio 1
	v_mfma_f32_16x16x32_bf16 v[54:57], v[174:177], v[192:195], v[54:57]
	v_mfma_f32_16x16x32_bf16 v[50:53], v[182:185], v[192:195], v[50:53]
	v_mfma_f32_16x16x32_bf16 v[30:33], v[174:177], v[200:203], v[30:33]
	v_mfma_f32_16x16x32_bf16 v[26:29], v[182:185], v[200:203], v[26:29]
	v_mfma_f32_16x16x32_bf16 v[42:45], v[174:177], v[208:211], v[42:45]
	v_mfma_f32_16x16x32_bf16 v[34:37], v[182:185], v[208:211], v[34:37]
	v_mfma_f32_16x16x32_bf16 v[22:25], v[174:177], v[216:219], v[22:25]
	v_mfma_f32_16x16x32_bf16 v[18:21], v[182:185], v[216:219], v[18:21]
	v_mfma_f32_16x16x32_bf16 v[54:57], v[178:181], v[196:199], v[54:57]
	v_mfma_f32_16x16x32_bf16 v[50:53], v[188:191], v[196:199], v[50:53]
	v_mfma_f32_16x16x32_bf16 v[30:33], v[178:181], v[204:207], v[30:33]
	v_mfma_f32_16x16x32_bf16 v[26:29], v[188:191], v[204:207], v[26:29]
	v_mfma_f32_16x16x32_bf16 v[42:45], v[178:181], v[212:215], v[42:45]
	v_mfma_f32_16x16x32_bf16 v[34:37], v[188:191], v[212:215], v[34:37]
	v_mfma_f32_16x16x32_bf16 v[22:25], v[178:181], v[220:223], v[22:25]
	v_mfma_f32_16x16x32_bf16 v[18:21], v[188:191], v[220:223], v[18:21]
	s_setprio 0
	s_barrier
	s_setprio 2
	s_add_i32 s50, 0, 0x18000
	v_add_u32_e32 v134, s50, v148
	s_add_i32 s51, 0, 0x1c000
	ds_read_b128 v[158:161], v134
	ds_read_b128 v[162:165], v134 offset:1024
	ds_read_b128 v[166:169], v134 offset:2048
	ds_read_b128 v[170:173], v134 offset:3072
	v_add_u32_e32 v134, s51, v148
	ds_read_b128 v[174:177], v134
	ds_read_b128 v[178:181], v134 offset:1024
	ds_read_b128 v[182:185], v134 offset:2048
	ds_read_b128 v[188:191], v134 offset:3072
	s_mov_b32 m0, s33
	ds_read_b128 v[192:195], v152 offset:32768
	ds_read_b128 v[196:199], v152 offset:33792
	ds_read_b128 v[200:203], v152 offset:34816
	ds_read_b128 v[204:207], v152 offset:35840
	ds_read_b128 v[208:211], v152 offset:36864
	ds_read_b128 v[212:215], v152 offset:37888
	ds_read_b128 v[216:219], v152 offset:38912
	ds_read_b128 v[220:223], v152 offset:39936
	global_load_lds_dwordx4 v137, s[26:27]
	s_mov_b32 m0, s34
	s_nop 0
	global_load_lds_dwordx4 v139, s[26:27]
	s_setprio 0
	s_waitcnt vmcnt(8)
	s_waitcnt lgkmcnt(0)
	s_barrier
	s_setprio 1
	s_waitcnt lgkmcnt(0)
	v_mfma_f32_16x16x32_bf16 v[126:129], v[158:161], v[192:195], v[126:129]
	v_mfma_f32_16x16x32_bf16 v[122:125], v[166:169], v[192:195], v[122:125]
	v_mfma_f32_16x16x32_bf16 v[110:113], v[158:161], v[200:203], v[110:113]
	v_mfma_f32_16x16x32_bf16 v[106:109], v[166:169], v[200:203], v[106:109]
	v_mfma_f32_16x16x32_bf16 v[94:97], v[158:161], v[208:211], v[94:97]
	v_mfma_f32_16x16x32_bf16 v[90:93], v[166:169], v[208:211], v[90:93]
	v_mfma_f32_16x16x32_bf16 v[78:81], v[158:161], v[216:219], v[78:81]
	v_mfma_f32_16x16x32_bf16 v[74:77], v[166:169], v[216:219], v[74:77]
	v_mfma_f32_16x16x32_bf16 v[126:129], v[162:165], v[196:199], v[126:129]
	v_mfma_f32_16x16x32_bf16 v[122:125], v[170:173], v[196:199], v[122:125]
	v_mfma_f32_16x16x32_bf16 v[110:113], v[162:165], v[204:207], v[110:113]
	v_mfma_f32_16x16x32_bf16 v[106:109], v[170:173], v[204:207], v[106:109]
	v_mfma_f32_16x16x32_bf16 v[94:97], v[162:165], v[212:215], v[94:97]
	v_mfma_f32_16x16x32_bf16 v[90:93], v[170:173], v[212:215], v[90:93]
	v_mfma_f32_16x16x32_bf16 v[78:81], v[162:165], v[220:223], v[78:81]
	v_mfma_f32_16x16x32_bf16 v[74:77], v[170:173], v[220:223], v[74:77]
	s_setprio 0
	s_setprio 1
	v_mfma_f32_16x16x32_bf16 v[118:121], v[174:177], v[192:195], v[118:121]
	v_mfma_f32_16x16x32_bf16 v[114:117], v[182:185], v[192:195], v[114:117]
	v_mfma_f32_16x16x32_bf16 v[102:105], v[174:177], v[200:203], v[102:105]
	v_mfma_f32_16x16x32_bf16 v[98:101], v[182:185], v[200:203], v[98:101]
	v_mfma_f32_16x16x32_bf16 v[86:89], v[174:177], v[208:211], v[86:89]
	v_mfma_f32_16x16x32_bf16 v[82:85], v[182:185], v[208:211], v[82:85]
	v_mfma_f32_16x16x32_bf16 v[70:73], v[174:177], v[216:219], v[70:73]
	v_mfma_f32_16x16x32_bf16 v[66:69], v[182:185], v[216:219], v[66:69]
	v_mfma_f32_16x16x32_bf16 v[118:121], v[178:181], v[196:199], v[118:121]
	v_mfma_f32_16x16x32_bf16 v[114:117], v[188:191], v[196:199], v[114:117]
	v_mfma_f32_16x16x32_bf16 v[102:105], v[178:181], v[204:207], v[102:105]
	v_mfma_f32_16x16x32_bf16 v[98:101], v[188:191], v[204:207], v[98:101]
	v_mfma_f32_16x16x32_bf16 v[86:89], v[178:181], v[212:215], v[86:89]
	v_mfma_f32_16x16x32_bf16 v[82:85], v[188:191], v[212:215], v[82:85]
	v_mfma_f32_16x16x32_bf16 v[70:73], v[178:181], v[220:223], v[70:73]
	v_mfma_f32_16x16x32_bf16 v[66:69], v[188:191], v[220:223], v[66:69]
	s_setprio 0
	s_barrier
; #define PG8_STAGE(bufoff, gbase, voff) do { _Pragma("unroll") for (int _i = 0; _i < 2; ++_i) \
;         __builtin_amdgcn_global_load_lds((const unsigned*)((const char*)(gbase) + (voff)[_i]), (PG8_LAS unsigned*)(lds + (bufoff) + ldsw + _i * 8192), 16, 0, 0); } while (0)
; #define PG8_LDA(dst, b, h) do { _Pragma("unroll") for (int m = 0; m < 4; ++m) _Pragma("unroll") for (int k = 0; k < 2; ++k) dst[m][k] = *(const PG8_LAS bf16x8*)(lds + PG8_SA(b, h) + aoff + m * 2048 + k * 1024); } while (0)
; #define PG8_MMA(ai, bj, At, Bt) do { __builtin_amdgcn_s_setprio(1); _Pragma("unroll") for (int m = 0; m < 4; ++m) _Pragma("unroll") for (int n = 0; n < 2; ++n) _Pragma("unroll") for (int k = 0; k < 2; ++k) \
;         acc[ai][bj][m][n] = __builtin_amdgcn_mfma_f32_16x16x32_bf16(Bt[n][k], At[m][k], acc[ai][bj][m][n], 0, 0, 0); __builtin_amdgcn_s_setprio(0); } while (0)
; #define PG8_WAIT_V(n) asm volatile("s_waitcnt vmcnt(" #n ")" ::: "memory")
; #define PG8_WAIT_L(n) asm volatile("s_waitcnt lgkmcnt(" #n ")" ::: "memory")
; #define PG8_BAR __builtin_amdgcn_s_barrier()
; #define PG8_SCHED __builtin_amdgcn_sched_barrier(0)
; #define PG8_STAGE(bufoff, gbase, voff) do { _Pragma("unroll") for (int _i = 0; _i < 2; ++_i) \
;         __builtin_amdgcn_global_load_lds((const unsigned*)((const char*)(gbase) + (voff)[_i]), (PG8_LAS unsigned*)(lds + (bufoff) + ldsw + _i * 8192), 16, 0, 0); } while (0)
; #define PG8_LDA(dst, b, h) do { _Pragma("unroll") for (int m = 0; m < 4; ++m) _Pragma("unroll") for (int k = 0; k < 2; ++k) dst[m][k] = *(const PG8_LAS bf16x8*)(lds + PG8_SA(b, h) + aoff + m * 2048 + k * 1024); } while (0)
; #define PG8_WAIT_V(n) asm volatile("s_waitcnt vmcnt(" #n ")" ::: "memory")
; #define PG8_WAIT_L(n) asm volatile("s_waitcnt lgkmcnt(" #n ")" ::: "memory")
; #define PG8_BAR __builtin_amdgcn_s_barrier()
; #define PG8_SCHED __builtin_amdgcn_sched_barrier(0)
; template <class Epi, class Sched>
; __device__ __forceinline__ void gemm_phase_gather(PG8_LAS unsigned char* lds, const Gemm g, const int* __restrict__ gidx, PG8_LAS int* itab  , const Sched& S, const Epi& E) {
;     ...
;             PG8_LDA(At, 1, 1); PG8_STAGE(PG8_SB(1, 0), b3, voffB); PG8_STAGE(PG8_SB(1, 1), b3 + hstep, voffB); PG8_STAGE(PG8_SA(1, 0), a3, vo2[0]);
;             PG8_WAIT_V(8); PG8_WAIT_L(0); PG8_BAR; PG8_MMA(1, 0, At, B0); PG8_MMA(1, 1, At, B1); PG8_BAR; PG8_SCHED;
;         }
	s_setprio 2
	s_add_i32 s26, s50, s28
	v_lshl_add_u64 v[226:227], v[226:227], 0, s[10:11]
	s_mov_b32 m0, s26
	ds_read_b128 v[192:195], v152 offset:49152
	ds_read_b128 v[196:199], v152 offset:50176
	ds_read_b128 v[200:203], v152 offset:51200
	ds_read_b128 v[204:207], v152 offset:52224
	ds_read_b128 v[208:211], v152 offset:53248
	ds_read_b128 v[212:215], v152 offset:54272
	ds_read_b128 v[216:219], v152 offset:55296
	ds_read_b128 v[220:223], v152 offset:56320
	global_load_lds_dwordx4 v[226:227], off
	s_add_i32 m0, s26, 0x2000
	s_add_u32 s24, s24, 0x80080
	v_lshl_add_u64 v[226:227], v[228:229], 0, s[10:11]
	s_addc_u32 s25, s25, 0
	s_add_i32 s26, s51, s28
	global_load_lds_dwordx4 v[226:227], off
	v_lshl_add_u64 v[226:227], s[24:25], 0, v[130:131]
	s_mov_b32 m0, s26
	v_lshl_add_u64 v[224:225], v[224:225], 0, s[10:11]
	global_load_lds_dwordx4 v[226:227], off
	v_lshl_add_u64 v[226:227], s[24:25], 0, v[132:133]
	s_add_i32 m0, s26, 0x2000
	s_nop 0
	global_load_lds_dwordx4 v[226:227], off
	v_lshl_add_u64 v[226:227], v[230:231], 0, s[10:11]
	s_mov_b32 m0, s35
	s_nop 0
	global_load_lds_dwordx4 v[226:227], off
	s_mov_b32 m0, s36
	s_nop 0
	global_load_lds_dwordx4 v[224:225], off
	s_setprio 0
	s_waitcnt vmcnt(8)
	s_waitcnt lgkmcnt(0)
	s_barrier
	s_setprio 1
	s_waitcnt lgkmcnt(0)
	v_mfma_f32_16x16x32_bf16 v[62:65], v[158:161], v[192:195], v[62:65]
	v_mfma_f32_16x16x32_bf16 v[58:61], v[166:169], v[192:195], v[58:61]
	v_mfma_f32_16x16x32_bf16 v[46:49], v[158:161], v[200:203], v[46:49]
	v_mfma_f32_16x16x32_bf16 v[38:41], v[166:169], v[200:203], v[38:41]
	v_mfma_f32_16x16x32_bf16 v[14:17], v[158:161], v[208:211], v[14:17]
	v_mfma_f32_16x16x32_bf16 v[10:13], v[166:169], v[208:211], v[10:13]
	v_mfma_f32_16x16x32_bf16 v[6:9], v[158:161], v[216:219], v[6:9]
	v_mfma_f32_16x16x32_bf16 v[2:5], v[166:169], v[216:219], v[2:5]
	v_mfma_f32_16x16x32_bf16 v[62:65], v[162:165], v[196:199], v[62:65]
	v_mfma_f32_16x16x32_bf16 v[58:61], v[170:173], v[196:199], v[58:61]
	v_mfma_f32_16x16x32_bf16 v[46:49], v[162:165], v[204:207], v[46:49]
	v_mfma_f32_16x16x32_bf16 v[38:41], v[170:173], v[204:207], v[38:41]
	v_mfma_f32_16x16x32_bf16 v[14:17], v[162:165], v[212:215], v[14:17]
	v_mfma_f32_16x16x32_bf16 v[10:13], v[170:173], v[212:215], v[10:13]
	v_mfma_f32_16x16x32_bf16 v[6:9], v[162:165], v[220:223], v[6:9]
	v_mfma_f32_16x16x32_bf16 v[2:5], v[170:173], v[220:223], v[2:5]
	s_setprio 0
	s_setprio 1
	v_mfma_f32_16x16x32_bf16 v[54:57], v[174:177], v[192:195], v[54:57]
	v_mfma_f32_16x16x32_bf16 v[50:53], v[182:185], v[192:195], v[50:53]
	v_mfma_f32_16x16x32_bf16 v[30:33], v[174:177], v[200:203], v[30:33]
	v_mfma_f32_16x16x32_bf16 v[26:29], v[182:185], v[200:203], v[26:29]
	v_mfma_f32_16x16x32_bf16 v[42:45], v[174:177], v[208:211], v[42:45]
	v_mfma_f32_16x16x32_bf16 v[34:37], v[182:185], v[208:211], v[34:37]
	v_mfma_f32_16x16x32_bf16 v[22:25], v[174:177], v[216:219], v[22:25]
	v_mfma_f32_16x16x32_bf16 v[18:21], v[182:185], v[216:219], v[18:21]
	v_mfma_f32_16x16x32_bf16 v[54:57], v[178:181], v[196:199], v[54:57]
	v_mfma_f32_16x16x32_bf16 v[50:53], v[188:191], v[196:199], v[50:53]
	v_mfma_f32_16x16x32_bf16 v[30:33], v[178:181], v[204:207], v[30:33]
	v_mfma_f32_16x16x32_bf16 v[26:29], v[188:191], v[204:207], v[26:29]
	v_mfma_f32_16x16x32_bf16 v[42:45], v[178:181], v[212:215], v[42:45]
	v_mfma_f32_16x16x32_bf16 v[34:37], v[188:191], v[212:215], v[34:37]
	v_mfma_f32_16x16x32_bf16 v[22:25], v[178:181], v[220:223], v[22:25]
	v_mfma_f32_16x16x32_bf16 v[18:21], v[188:191], v[220:223], v[18:21]
	s_setprio 0
	s_barrier
	s_setprio 2
	s_add_i32 s49, s49, 2
	s_add_u32 s22, s22, 0x100
	s_addc_u32 s23, s23, 0
	s_cmp_gt_u32 s49, 29
	s_cbranch_scc0 .LBB0_1278
	s_and_b64 vcc, exec, s[14:15]
	s_cbranch_vccz .LBB0_1281
	s_barrier

; #define PG8_STAGE(bufoff, gbase, voff) do { _Pragma("unroll") for (int _i = 0; _i < 2; ++_i) \
;         __builtin_amdgcn_global_load_lds((const unsigned*)((const char*)(gbase) + (voff)[_i]), (PG8_LAS unsigned*)(lds + (bufoff) + ldsw + _i * 8192), 16, 0, 0); } while (0)
; #define PG8_LDA(dst, b, h) do { _Pragma("unroll") for (int m = 0; m < 4; ++m) _Pragma("unroll") for (int k = 0; k < 2; ++k) dst[m][k] = *(const PG8_LAS bf16x8*)(lds + PG8_SA(b, h) + aoff + m * 2048 + k * 1024); } while (0)
; #define PG8_LDB(dst, b, h) do { _Pragma("unroll") for (int n = 0; n < 2; ++n) _Pragma("unroll") for (int k = 0; k < 2; ++k) dst[n][k] = *(const PG8_LAS bf16x8*)(lds + PG8_SB(b, h) + boff + n * 2048 + k * 1024); } while (0)
; #define PG8_MMA(ai, bj, At, Bt) do { __builtin_amdgcn_s_setprio(1); _Pragma("unroll") for (int m = 0; m < 4; ++m) _Pragma("unroll") for (int n = 0; n < 2; ++n) _Pragma("unroll") for (int k = 0; k < 2; ++k) \
;         acc[ai][bj][m][n] = __builtin_amdgcn_mfma_f32_16x16x32_bf16(Bt[n][k], At[m][k], acc[ai][bj][m][n], 0, 0, 0); __builtin_amdgcn_s_setprio(0); } while (0)
; #define PG8_WAIT_V(n) asm volatile("s_waitcnt vmcnt(" #n ")" ::: "memory")
; #define PG8_WAIT_L(n) asm volatile("s_waitcnt lgkmcnt(" #n ")" ::: "memory")
; #define PG8_BAR __builtin_amdgcn_s_barrier()
; template <class Epi, class Sched, bool ALIGN_EPI = false, bool SP2 = false>
; __device__ __forceinline__ void gemm_phase(PG8_LAS unsigned char* lds, const Gemm g, const Sched& S, const Epi& E) {
;     ...
;             const char* a1 = cA + (size_t)(t + 1) * kstep;
;             const char* a2 = last ? nA : cA + (size_t)(t + 2) * kstep; const char* b2 = last ? nB : cB + (size_t)(t + 2) * kstep;
;             const char* a3 = a2 + kstep; const char* b3 = b2 + kstep;
;             if (last && has_next) S.a_ready(nxt);
;             if constexpr (SP2) {
;             PG8_LDB(B0, 0, 0); PG8_LDB(B1, 0, 1); PG8_SCHED; PG8_LDA(At, 0, 0); PG8_STAGE(PG8_SA(1, 1), a1 + hstep, voffA);
;             PG8_WAIT_V(8); PG8_WAIT_L(0); PG8_BAR; PG8_MMA(0, 0, At, B0); PG8_MMA(0, 1, At, B1); PG8_BAR; PG8_SCHED;
;             PG8_LDA(At, 0, 1); PG8_STAGE(PG8_SB(0, 0), b2, voffB); PG8_STAGE(PG8_SB(0, 1), b2 + hstep, voffB); PG8_STAGE(PG8_SA(0, 0), a2, voffA);
;             PG8_WAIT_V(8); PG8_WAIT_L(0); PG8_BAR; PG8_MMA(1, 0, At, B0); PG8_MMA(1, 1, At, B1); PG8_BAR; PG8_SCHED;
.LBB0_1349:
	s_setprio 2
	ds_read_b128 v[152:155], v148
	ds_read_b128 v[156:159], v148 offset:1024
	ds_read_b128 v[160:163], v148 offset:2048
	ds_read_b128 v[164:167], v148 offset:3072
	ds_read_b128 v[168:171], v149
	ds_read_b128 v[172:175], v149 offset:1024
	ds_read_b128 v[176:179], v149 offset:2048
	ds_read_b128 v[180:183], v149 offset:3072
	s_add_u32 s36, s34, 0xfff80080
	s_addc_u32 s37, s35, -1
	s_cmp_eq_u32 s59, 28
	s_cselect_b32 s39, s19, s37
	s_cselect_b32 s38, s55, s36
	s_cselect_b32 s37, s21, s58
	s_cselect_b32 s36, s56, s57
	v_lshl_add_u64 v[144:145], s[34:35], 0, v[138:139]
	s_add_i32 m0, s29, 0xc000
	ds_read_b128 v[188:191], v150
	ds_read_b128 v[192:195], v150 offset:1024
	ds_read_b128 v[196:199], v150 offset:2048
	ds_read_b128 v[200:203], v150 offset:3072
	ds_read_b128 v[204:207], v150 offset:4096
	ds_read_b128 v[208:211], v150 offset:5120
	ds_read_b128 v[212:215], v150 offset:6144
	ds_read_b128 v[216:219], v150 offset:7168
	global_load_lds_dwordx4 v[144:145], off
	v_lshl_add_u64 v[144:145], s[34:35], 0, v[140:141]
	s_add_i32 m0, s29, 0xe000
	s_nop 0
	global_load_lds_dwordx4 v[144:145], off
	s_setprio 0
	s_waitcnt vmcnt(8)
	s_waitcnt lgkmcnt(0)
	s_barrier
	s_setprio 1
	s_waitcnt lgkmcnt(0)
	v_mfma_f32_16x16x32_bf16 v[124:127], v[152:155], v[188:191], v[124:127]
	v_mfma_f32_16x16x32_bf16 v[120:123], v[160:163], v[188:191], v[120:123]
	v_mfma_f32_16x16x32_bf16 v[116:119], v[152:155], v[196:199], v[116:119]
	v_mfma_f32_16x16x32_bf16 v[112:115], v[160:163], v[196:199], v[112:115]
	v_mfma_f32_16x16x32_bf16 v[100:103], v[152:155], v[204:207], v[100:103]
	v_mfma_f32_16x16x32_bf16 v[96:99], v[160:163], v[204:207], v[96:99]
	v_mfma_f32_16x16x32_bf16 v[76:79], v[152:155], v[212:215], v[76:79]
	v_mfma_f32_16x16x32_bf16 v[72:75], v[160:163], v[212:215], v[72:75]
	v_mfma_f32_16x16x32_bf16 v[124:127], v[156:159], v[192:195], v[124:127]
	v_mfma_f32_16x16x32_bf16 v[120:123], v[164:167], v[192:195], v[120:123]
	v_mfma_f32_16x16x32_bf16 v[116:119], v[156:159], v[200:203], v[116:119]
	v_mfma_f32_16x16x32_bf16 v[112:115], v[164:167], v[200:203], v[112:115]
	v_mfma_f32_16x16x32_bf16 v[100:103], v[156:159], v[208:211], v[100:103]
	v_mfma_f32_16x16x32_bf16 v[96:99], v[164:167], v[208:211], v[96:99]
	v_mfma_f32_16x16x32_bf16 v[76:79], v[156:159], v[216:219], v[76:79]
	v_mfma_f32_16x16x32_bf16 v[72:75], v[164:167], v[216:219], v[72:75]
	s_setprio 0
	s_setprio 1
	v_mfma_f32_16x16x32_bf16 v[108:111], v[168:171], v[188:191], v[108:111]
	v_mfma_f32_16x16x32_bf16 v[104:107], v[176:179], v[188:191], v[104:107]
	v_mfma_f32_16x16x32_bf16 v[92:95], v[168:171], v[196:199], v[92:95]
	v_mfma_f32_16x16x32_bf16 v[88:91], v[176:179], v[196:199], v[88:91]
	v_mfma_f32_16x16x32_bf16 v[84:87], v[168:171], v[204:207], v[84:87]
	v_mfma_f32_16x16x32_bf16 v[80:83], v[176:179], v[204:207], v[80:83]
	v_mfma_f32_16x16x32_bf16 v[68:71], v[168:171], v[212:215], v[68:71]
	v_mfma_f32_16x16x32_bf16 v[64:67], v[176:179], v[212:215], v[64:67]
	v_mfma_f32_16x16x32_bf16 v[108:111], v[172:175], v[192:195], v[108:111]
	v_mfma_f32_16x16x32_bf16 v[104:107], v[180:183], v[192:195], v[104:107]
	v_mfma_f32_16x16x32_bf16 v[92:95], v[172:175], v[200:203], v[92:95]
	v_mfma_f32_16x16x32_bf16 v[88:91], v[180:183], v[200:203], v[88:91]
	v_mfma_f32_16x16x32_bf16 v[84:87], v[172:175], v[208:211], v[84:87]
	v_mfma_f32_16x16x32_bf16 v[80:83], v[180:183], v[208:211], v[80:83]
	v_mfma_f32_16x16x32_bf16 v[68:71], v[172:175], v[216:219], v[68:71]
	v_mfma_f32_16x16x32_bf16 v[64:67], v[180:183], v[216:219], v[64:67]
	s_setprio 0
	s_barrier
	s_setprio 2
	s_add_i32 s60, s49, s43
	v_lshl_add_u64 v[144:145], s[36:37], 0, v[132:133]
	s_mov_b32 m0, s60
	ds_read_b128 v[188:191], v150 offset:16384
	ds_read_b128 v[192:195], v150 offset:17408
	ds_read_b128 v[196:199], v150 offset:18432
	ds_read_b128 v[200:203], v150 offset:19456
	ds_read_b128 v[204:207], v150 offset:20480
	ds_read_b128 v[208:211], v150 offset:21504
	ds_read_b128 v[212:215], v150 offset:22528
	ds_read_b128 v[216:219], v150 offset:23552
	global_load_lds_dwordx4 v[144:145], off
	s_add_i32 m0, s60, 0x2000
	s_add_u32 s60, s36, 0x80000
	v_lshl_add_u64 v[184:185], s[36:37], 0, v[128:129]
	s_addc_u32 s61, s37, 0
	s_add_i32 s62, s50, s43
	global_load_lds_dwordx4 v[184:185], off
	v_lshl_add_u64 v[220:221], s[60:61], 0, v[132:133]
	s_mov_b32 m0, s62
	v_lshl_add_u64 v[222:223], s[38:39], 0, v[130:131]
	global_load_lds_dwordx4 v[220:221], off
	v_lshl_add_u64 v[220:221], s[60:61], 0, v[128:129]
	s_add_i32 m0, s62, 0x2000
	s_nop 0
	global_load_lds_dwordx4 v[220:221], off
	v_lshl_add_u64 v[220:221], s[38:39], 0, v[134:135]
	s_mov_b32 m0, s29
	s_nop 0
	global_load_lds_dwordx4 v[220:221], off
	s_mov_b32 m0, s31
	s_nop 0
	global_load_lds_dwordx4 v[222:223], off
	s_setprio 0
	s_waitcnt vmcnt(8)
	s_waitcnt lgkmcnt(0)
	s_barrier
; #define PG8_STAGE(bufoff, gbase, voff) do { _Pragma("unroll") for (int _i = 0; _i < 2; ++_i) \
;         __builtin_amdgcn_global_load_lds((const unsigned*)((const char*)(gbase) + (voff)[_i]), (PG8_LAS unsigned*)(lds + (bufoff) + ldsw + _i * 8192), 16, 0, 0); } while (0)
; #define PG8_LDA(dst, b, h) do { _Pragma("unroll") for (int m = 0; m < 4; ++m) _Pragma("unroll") for (int k = 0; k < 2; ++k) dst[m][k] = *(const PG8_LAS bf16x8*)(lds + PG8_SA(b, h) + aoff + m * 2048 + k * 1024); } while (0)
; #define PG8_LDB(dst, b, h) do { _Pragma("unroll") for (int n = 0; n < 2; ++n) _Pragma("unroll") for (int k = 0; k < 2; ++k) dst[n][k] = *(const PG8_LAS bf16x8*)(lds + PG8_SB(b, h) + boff + n * 2048 + k * 1024); } while (0)
; #define PG8_MMA(ai, bj, At, Bt) do { __builtin_amdgcn_s_setprio(1); _Pragma("unroll") for (int m = 0; m < 4; ++m) _Pragma("unroll") for (int n = 0; n < 2; ++n) _Pragma("unroll") for (int k = 0; k < 2; ++k) \
;         acc[ai][bj][m][n] = __builtin_amdgcn_mfma_f32_16x16x32_bf16(Bt[n][k], At[m][k], acc[ai][bj][m][n], 0, 0, 0); __builtin_amdgcn_s_setprio(0); } while (0)
; #define PG8_WAIT_V(n) asm volatile("s_waitcnt vmcnt(" #n ")" ::: "memory")
; #define PG8_WAIT_L(n) asm volatile("s_waitcnt lgkmcnt(" #n ")" ::: "memory")
; #define PG8_BAR __builtin_amdgcn_s_barrier()
; #define PG8_SCHED __builtin_amdgcn_sched_barrier(0)
; #define PG8_STAGE(bufoff, gbase, voff) do { _Pragma("unroll") for (int _i = 0; _i < 2; ++_i) \
;         __builtin_amdgcn_global_load_lds((const unsigned*)((const char*)(gbase) + (voff)[_i]), (PG8_LAS unsigned*)(lds + (bufoff) + ldsw + _i * 8192), 16, 0, 0); } while (0)
; #define PG8_WAIT_V(n) asm volatile("s_waitcnt vmcnt(" #n ")" ::: "memory")
; #define PG8_WAIT_L(n) asm volatile("s_waitcnt lgkmcnt(" #n ")" ::: "memory")
; #define PG8_BAR __builtin_amdgcn_s_barrier()
; template <class Epi, class Sched, bool ALIGN_EPI = false, bool SP2 = false>
; __device__ __forceinline__ void gemm_phase(PG8_LAS unsigned char* lds, const Gemm g, const Sched& S, const Epi& E) {
;     ...
;             PG8_WAIT_V(8); PG8_WAIT_L(0); PG8_BAR; PG8_MMA(1, 0, At, B0); PG8_MMA(1, 1, At, B1); PG8_BAR; PG8_SCHED;
;             PG8_LDB(B0, 1, 0); PG8_LDB(B1, 1, 1); PG8_SCHED; PG8_LDA(At, 1, 0); PG8_STAGE(PG8_SA(0, 1), a2 + hstep, voffA);
;             PG8_WAIT_V(8); PG8_WAIT_L(0); PG8_BAR; PG8_MMA(0, 0, At, B0); PG8_MMA(0, 1, At, B1); PG8_BAR; PG8_SCHED;
	s_setprio 1
	s_waitcnt lgkmcnt(0)
	v_mfma_f32_16x16x32_bf16 v[60:63], v[152:155], v[188:191], v[60:63]
	v_mfma_f32_16x16x32_bf16 v[56:59], v[160:163], v[188:191], v[56:59]
	v_mfma_f32_16x16x32_bf16 v[52:55], v[152:155], v[196:199], v[52:55]
	v_mfma_f32_16x16x32_bf16 v[44:47], v[160:163], v[196:199], v[44:47]
	v_mfma_f32_16x16x32_bf16 v[36:39], v[152:155], v[204:207], v[36:39]
	v_mfma_f32_16x16x32_bf16 v[28:31], v[160:163], v[204:207], v[28:31]
	v_mfma_f32_16x16x32_bf16 v[20:23], v[152:155], v[212:215], v[20:23]
	v_mfma_f32_16x16x32_bf16 v[12:15], v[160:163], v[212:215], v[12:15]
	v_mfma_f32_16x16x32_bf16 v[60:63], v[156:159], v[192:195], v[60:63]
	v_mfma_f32_16x16x32_bf16 v[56:59], v[164:167], v[192:195], v[56:59]
	v_mfma_f32_16x16x32_bf16 v[52:55], v[156:159], v[200:203], v[52:55]
	v_mfma_f32_16x16x32_bf16 v[44:47], v[164:167], v[200:203], v[44:47]
	v_mfma_f32_16x16x32_bf16 v[36:39], v[156:159], v[208:211], v[36:39]
	v_mfma_f32_16x16x32_bf16 v[28:31], v[164:167], v[208:211], v[28:31]
	v_mfma_f32_16x16x32_bf16 v[20:23], v[156:159], v[216:219], v[20:23]
	v_mfma_f32_16x16x32_bf16 v[12:15], v[164:167], v[216:219], v[12:15]
	s_setprio 0
	s_setprio 1
	v_mfma_f32_16x16x32_bf16 v[48:51], v[168:171], v[188:191], v[48:51]
	v_mfma_f32_16x16x32_bf16 v[40:43], v[176:179], v[188:191], v[40:43]
	v_mfma_f32_16x16x32_bf16 v[32:35], v[168:171], v[196:199], v[32:35]
	v_mfma_f32_16x16x32_bf16 v[24:27], v[176:179], v[196:199], v[24:27]
	v_mfma_f32_16x16x32_bf16 v[16:19], v[168:171], v[204:207], v[16:19]
	v_mfma_f32_16x16x32_bf16 v[8:11], v[176:179], v[204:207], v[8:11]
	v_mfma_f32_16x16x32_bf16 v[4:7], v[168:171], v[212:215], v[4:7]
	v_mfma_f32_16x16x32_bf16 v[0:3], v[176:179], v[212:215], v[0:3]
	v_mfma_f32_16x16x32_bf16 v[48:51], v[172:175], v[192:195], v[48:51]
	v_mfma_f32_16x16x32_bf16 v[40:43], v[180:183], v[192:195], v[40:43]
	v_mfma_f32_16x16x32_bf16 v[32:35], v[172:175], v[200:203], v[32:35]
	v_mfma_f32_16x16x32_bf16 v[24:27], v[180:183], v[200:203], v[24:27]
	v_mfma_f32_16x16x32_bf16 v[16:19], v[172:175], v[208:211], v[16:19]
	v_mfma_f32_16x16x32_bf16 v[8:11], v[180:183], v[208:211], v[8:11]
	v_mfma_f32_16x16x32_bf16 v[4:7], v[172:175], v[216:219], v[4:7]
	v_mfma_f32_16x16x32_bf16 v[0:3], v[180:183], v[216:219], v[0:3]
	s_setprio 0
	s_barrier
	s_setprio 2
	s_add_i32 s60, 0, 0x18000
	v_add_u32_e32 v136, s60, v146
	s_add_i32 s61, 0, 0x1c000
	ds_read_b128 v[152:155], v136
	ds_read_b128 v[156:159], v136 offset:1024
	ds_read_b128 v[160:163], v136 offset:2048
	ds_read_b128 v[164:167], v136 offset:3072
	v_add_u32_e32 v136, s61, v146
	ds_read_b128 v[168:171], v136
	ds_read_b128 v[172:175], v136 offset:1024
	ds_read_b128 v[176:179], v136 offset:2048
	ds_read_b128 v[180:183], v136 offset:3072
	s_add_u32 s38, s38, 0x80000
	s_addc_u32 s39, s39, 0
	s_mov_b32 m0, s44
	v_lshl_add_u64 v[224:225], s[38:39], 0, v[134:135]
	ds_read_b128 v[188:191], v150 offset:32768
	ds_read_b128 v[192:195], v150 offset:33792
	ds_read_b128 v[196:199], v150 offset:34816
	ds_read_b128 v[200:203], v150 offset:35840
	ds_read_b128 v[204:207], v150 offset:36864
	ds_read_b128 v[208:211], v150 offset:37888
	ds_read_b128 v[212:215], v150 offset:38912
	ds_read_b128 v[216:219], v150 offset:39936
	global_load_lds_dwordx4 v[224:225], off
	v_lshl_add_u64 v[224:225], s[38:39], 0, v[130:131]
	s_mov_b32 m0, s45
	s_nop 0
	global_load_lds_dwordx4 v[224:225], off
	s_setprio 0
	s_waitcnt vmcnt(8)
	s_waitcnt lgkmcnt(0)
	s_barrier
	s_setprio 1
	s_waitcnt lgkmcnt(0)
	v_mfma_f32_16x16x32_bf16 v[124:127], v[152:155], v[188:191], v[124:127]
	v_mfma_f32_16x16x32_bf16 v[120:123], v[160:163], v[188:191], v[120:123]
	v_mfma_f32_16x16x32_bf16 v[116:119], v[152:155], v[196:199], v[116:119]
	v_mfma_f32_16x16x32_bf16 v[112:115], v[160:163], v[196:199], v[112:115]
	v_mfma_f32_16x16x32_bf16 v[100:103], v[152:155], v[204:207], v[100:103]
	v_mfma_f32_16x16x32_bf16 v[96:99], v[160:163], v[204:207], v[96:99]
	v_mfma_f32_16x16x32_bf16 v[76:79], v[152:155], v[212:215], v[76:79]
	v_mfma_f32_16x16x32_bf16 v[72:75], v[160:163], v[212:215], v[72:75]
	v_mfma_f32_16x16x32_bf16 v[124:127], v[156:159], v[192:195], v[124:127]
	v_mfma_f32_16x16x32_bf16 v[120:123], v[164:167], v[192:195], v[120:123]
	v_mfma_f32_16x16x32_bf16 v[116:119], v[156:159], v[200:203], v[116:119]
	v_mfma_f32_16x16x32_bf16 v[112:115], v[164:167], v[200:203], v[112:115]
	v_mfma_f32_16x16x32_bf16 v[100:103], v[156:159], v[208:211], v[100:103]
	v_mfma_f32_16x16x32_bf16 v[96:99], v[164:167], v[208:211], v[96:99]
	v_mfma_f32_16x16x32_bf16 v[76:79], v[156:159], v[216:219], v[76:79]
	v_mfma_f32_16x16x32_bf16 v[72:75], v[164:167], v[216:219], v[72:75]
	s_setprio 0
	s_setprio 1
	v_mfma_f32_16x16x32_bf16 v[108:111], v[168:171], v[188:191], v[108:111]
	v_mfma_f32_16x16x32_bf16 v[104:107], v[176:179], v[188:191], v[104:107]
	v_mfma_f32_16x16x32_bf16 v[92:95], v[168:171], v[196:199], v[92:95]
	v_mfma_f32_16x16x32_bf16 v[88:91], v[176:179], v[196:199], v[88:91]
	v_mfma_f32_16x16x32_bf16 v[84:87], v[168:171], v[204:207], v[84:87]
	v_mfma_f32_16x16x32_bf16 v[80:83], v[176:179], v[204:207], v[80:83]
	v_mfma_f32_16x16x32_bf16 v[68:71], v[168:171], v[212:215], v[68:71]
	v_mfma_f32_16x16x32_bf16 v[64:67], v[176:179], v[212:215], v[64:67]
	v_mfma_f32_16x16x32_bf16 v[108:111], v[172:175], v[192:195], v[108:111]
	v_mfma_f32_16x16x32_bf16 v[104:107], v[180:183], v[192:195], v[104:107]
	v_mfma_f32_16x16x32_bf16 v[92:95], v[172:175], v[200:203], v[92:95]
	v_mfma_f32_16x16x32_bf16 v[88:91], v[180:183], v[200:203], v[88:91]
	v_mfma_f32_16x16x32_bf16 v[84:87], v[172:175], v[208:211], v[84:87]
	v_mfma_f32_16x16x32_bf16 v[80:83], v[180:183], v[208:211], v[80:83]
	v_mfma_f32_16x16x32_bf16 v[68:71], v[172:175], v[216:219], v[68:71]
	v_mfma_f32_16x16x32_bf16 v[64:67], v[180:183], v[216:219], v[64:67]
	s_setprio 0
	s_barrier
; #define PG8_STAGE(bufoff, gbase, voff) do { _Pragma("unroll") for (int _i = 0; _i < 2; ++_i) \
;         __builtin_amdgcn_global_load_lds((const unsigned*)((const char*)(gbase) + (voff)[_i]), (PG8_LAS unsigned*)(lds + (bufoff) + ldsw + _i * 8192), 16, 0, 0); } while (0)
; #define PG8_LDA(dst, b, h) do { _Pragma("unroll") for (int m = 0; m < 4; ++m) _Pragma("unroll") for (int k = 0; k < 2; ++k) dst[m][k] = *(const PG8_LAS bf16x8*)(lds + PG8_SA(b, h) + aoff + m * 2048 + k * 1024); } while (0)
; #define PG8_MMA(ai, bj, At, Bt) do { __builtin_amdgcn_s_setprio(1); _Pragma("unroll") for (int m = 0; m < 4; ++m) _Pragma("unroll") for (int n = 0; n < 2; ++n) _Pragma("unroll") for (int k = 0; k < 2; ++k) \
;         acc[ai][bj][m][n] = __builtin_amdgcn_mfma_f32_16x16x32_bf16(Bt[n][k], At[m][k], acc[ai][bj][m][n], 0, 0, 0); __builtin_amdgcn_s_setprio(0); } while (0)
; #define PG8_WAIT_V(n) asm volatile("s_waitcnt vmcnt(" #n ")" ::: "memory")
; #define PG8_WAIT_L(n) asm volatile("s_waitcnt lgkmcnt(" #n ")" ::: "memory")
; #define PG8_BAR __builtin_amdgcn_s_barrier()
; #define PG8_SCHED __builtin_amdgcn_sched_barrier(0)
; #define PG8_STAGE(bufoff, gbase, voff) do { _Pragma("unroll") for (int _i = 0; _i < 2; ++_i) \
;         __builtin_amdgcn_global_load_lds((const unsigned*)((const char*)(gbase) + (voff)[_i]), (PG8_LAS unsigned*)(lds + (bufoff) + ldsw + _i * 8192), 16, 0, 0); } while (0)
; #define PG8_LDA(dst, b, h) do { _Pragma("unroll") for (int m = 0; m < 4; ++m) _Pragma("unroll") for (int k = 0; k < 2; ++k) dst[m][k] = *(const PG8_LAS bf16x8*)(lds + PG8_SA(b, h) + aoff + m * 2048 + k * 1024); } while (0)
; #define PG8_WAIT_V(n) asm volatile("s_waitcnt vmcnt(" #n ")" ::: "memory")
; #define PG8_WAIT_L(n) asm volatile("s_waitcnt lgkmcnt(" #n ")" ::: "memory")
; #define PG8_BAR __builtin_amdgcn_s_barrier()
; #define PG8_SCHED __builtin_amdgcn_sched_barrier(0)
; template <class Epi, class Sched, bool ALIGN_EPI = false, bool SP2 = false>
; __device__ __forceinline__ void gemm_phase(PG8_LAS unsigned char* lds, const Gemm g, const Sched& S, const Epi& E) {
;     ...
;             PG8_LDA(At, 1, 1); PG8_STAGE(PG8_SB(1, 0), b3, voffB); PG8_STAGE(PG8_SB(1, 1), b3 + hstep, voffB); PG8_STAGE(PG8_SA(1, 0), a3, voffA);
;             PG8_WAIT_V(8); PG8_WAIT_L(0); PG8_BAR; PG8_MMA(1, 0, At, B0); PG8_MMA(1, 1, At, B1); PG8_BAR; PG8_SCHED;
	s_setprio 2
	s_add_i32 s38, s60, s43
	v_lshl_add_u64 v[144:145], v[144:145], 0, s[8:9]
	s_mov_b32 m0, s38
	ds_read_b128 v[188:191], v150 offset:49152
	ds_read_b128 v[192:195], v150 offset:50176
	ds_read_b128 v[196:199], v150 offset:51200
	ds_read_b128 v[200:203], v150 offset:52224
	ds_read_b128 v[204:207], v150 offset:53248
	ds_read_b128 v[208:211], v150 offset:54272
	ds_read_b128 v[212:215], v150 offset:55296
	ds_read_b128 v[216:219], v150 offset:56320
	global_load_lds_dwordx4 v[144:145], off
	s_add_i32 m0, s38, 0x2000
	s_add_u32 s36, s36, 0x80080
	v_lshl_add_u64 v[144:145], v[184:185], 0, s[8:9]
	s_addc_u32 s37, s37, 0
	s_add_i32 s38, s61, s43
	global_load_lds_dwordx4 v[144:145], off
	v_lshl_add_u64 v[144:145], s[36:37], 0, v[132:133]
	s_mov_b32 m0, s38
	s_nop 0
	global_load_lds_dwordx4 v[144:145], off
	v_lshl_add_u64 v[144:145], s[36:37], 0, v[128:129]
	s_add_i32 m0, s38, 0x2000
	s_nop 0
	global_load_lds_dwordx4 v[144:145], off
	v_lshl_add_u64 v[144:145], v[220:221], 0, s[8:9]
	s_mov_b32 m0, s47
	s_nop 0
	global_load_lds_dwordx4 v[144:145], off
	v_lshl_add_u64 v[144:145], v[222:223], 0, s[8:9]
	s_mov_b32 m0, s48
	s_nop 0
	global_load_lds_dwordx4 v[144:145], off
	s_setprio 0
	s_waitcnt vmcnt(8)
	s_waitcnt lgkmcnt(0)
	s_barrier
	s_setprio 1
	s_waitcnt lgkmcnt(0)
	v_mfma_f32_16x16x32_bf16 v[60:63], v[152:155], v[188:191], v[60:63]
	v_mfma_f32_16x16x32_bf16 v[56:59], v[160:163], v[188:191], v[56:59]
	v_mfma_f32_16x16x32_bf16 v[52:55], v[152:155], v[196:199], v[52:55]
	v_mfma_f32_16x16x32_bf16 v[44:47], v[160:163], v[196:199], v[44:47]
	v_mfma_f32_16x16x32_bf16 v[36:39], v[152:155], v[204:207], v[36:39]
	v_mfma_f32_16x16x32_bf16 v[28:31], v[160:163], v[204:207], v[28:31]
	v_mfma_f32_16x16x32_bf16 v[20:23], v[152:155], v[212:215], v[20:23]
	v_mfma_f32_16x16x32_bf16 v[12:15], v[160:163], v[212:215], v[12:15]
	v_mfma_f32_16x16x32_bf16 v[60:63], v[156:159], v[192:195], v[60:63]
	v_mfma_f32_16x16x32_bf16 v[56:59], v[164:167], v[192:195], v[56:59]
	v_mfma_f32_16x16x32_bf16 v[52:55], v[156:159], v[200:203], v[52:55]
	v_mfma_f32_16x16x32_bf16 v[44:47], v[164:167], v[200:203], v[44:47]
	v_mfma_f32_16x16x32_bf16 v[36:39], v[156:159], v[208:211], v[36:39]
	v_mfma_f32_16x16x32_bf16 v[28:31], v[164:167], v[208:211], v[28:31]
	v_mfma_f32_16x16x32_bf16 v[20:23], v[156:159], v[216:219], v[20:23]
	v_mfma_f32_16x16x32_bf16 v[12:15], v[164:167], v[216:219], v[12:15]
	s_setprio 0
	s_setprio 1
	v_mfma_f32_16x16x32_bf16 v[48:51], v[168:171], v[188:191], v[48:51]
	v_mfma_f32_16x16x32_bf16 v[40:43], v[176:179], v[188:191], v[40:43]
	v_mfma_f32_16x16x32_bf16 v[32:35], v[168:171], v[196:199], v[32:35]
	v_mfma_f32_16x16x32_bf16 v[24:27], v[176:179], v[196:199], v[24:27]
	v_mfma_f32_16x16x32_bf16 v[16:19], v[168:171], v[204:207], v[16:19]
	v_mfma_f32_16x16x32_bf16 v[8:11], v[176:179], v[204:207], v[8:11]
	v_mfma_f32_16x16x32_bf16 v[4:7], v[168:171], v[212:215], v[4:7]
	v_mfma_f32_16x16x32_bf16 v[0:3], v[176:179], v[212:215], v[0:3]
	v_mfma_f32_16x16x32_bf16 v[48:51], v[172:175], v[192:195], v[48:51]
	v_mfma_f32_16x16x32_bf16 v[40:43], v[180:183], v[192:195], v[40:43]
	v_mfma_f32_16x16x32_bf16 v[32:35], v[172:175], v[200:203], v[32:35]
	v_mfma_f32_16x16x32_bf16 v[24:27], v[180:183], v[200:203], v[24:27]
	v_mfma_f32_16x16x32_bf16 v[16:19], v[172:175], v[208:211], v[16:19]
	v_mfma_f32_16x16x32_bf16 v[8:11], v[180:183], v[208:211], v[8:11]
	v_mfma_f32_16x16x32_bf16 v[4:7], v[172:175], v[216:219], v[4:7]
	v_mfma_f32_16x16x32_bf16 v[0:3], v[180:183], v[216:219], v[0:3]
	s_setprio 0
	s_barrier
	s_setprio 2
	s_add_i32 s59, s59, 2
	s_add_u32 s34, s34, 0x100
	s_addc_u32 s35, s35, 0
	s_add_u32 s57, s57, 0x100
	s_addc_u32 s58, s58, 0
	s_cmp_gt_u32 s59, 29
	s_cbranch_scc0 .LBB0_1349
	s_and_b64 vcc, exec, s[10:11]
	s_cbranch_vccz .LBB0_1352
	s_barrier
